# GEMM loops: per-phase s_setprio 1/0 flips removed (A/B of the priority toggling)
# speedup vs baseline: 1.0081x; 1.0062x over previous
.LBB0_371:
	s_add_i32 s31, s24, 2
	s_add_u32 s45, s56, s29
	s_addc_u32 s25, s57, s30
	s_add_i32 s64, 0, 0x10000
	v_add_u32_e32 v0, s64, v139
	s_add_u32 s66, s20, s29
	ds_read_b128 v[146:149], v0
	ds_read_b128 v[150:153], v0 offset:1024
	ds_read_b128 v[154:157], v0 offset:2048
	ds_read_b128 v[158:161], v0 offset:3072
	s_addc_u32 s67, s21, s30
	s_add_u32 s66, s66, 0xffffff80
	s_addc_u32 s67, s67, -1
	s_add_i32 s71, s64, s26
	s_add_i32 m0, s46, 0xc000
	s_add_i32 s70, s46, 0xe000
	s_add_i32 s81, 0, 0x14000
	s_add_i32 s84, s71, 0x2000
	s_cmp_eq_u32 s79, s24
	s_cselect_b32 s24, s42, s45
	s_cselect_b32 s25, s43, s25
	s_cselect_b32 s45, 0, s30
	s_cselect_b32 s64, 0, s29
	v_mov_b32_e32 v0, v134
	ds_read_b128 v[162:165], v141
	ds_read_b128 v[166:169], v141 offset:1024
	ds_read_b128 v[170:173], v141 offset:2048
	ds_read_b128 v[190:193], v141 offset:3072
	ds_read_b128 v[194:197], v141 offset:4096
	ds_read_b128 v[198:201], v141 offset:5120
	ds_read_b128 v[202:205], v141 offset:6144
	ds_read_b128 v[206:209], v141 offset:7168
	s_nop 0
	global_load_lds_dwordx4 v0, s[66:67]
	v_mov_b32_e32 v0, v136
	s_mov_b32 m0, s70
	s_nop 0
	global_load_lds_dwordx4 v0, s[66:67]
	s_waitcnt lgkmcnt(8)
	s_barrier
	s_waitcnt lgkmcnt(0)
	s_waitcnt lgkmcnt(0)
	v_mfma_f32_16x16x32_bf16 v[120:123], v[146:149], v[162:165], v[120:123]
	v_mfma_f32_16x16x32_bf16 v[116:119], v[154:157], v[162:165], v[116:119]
	v_mfma_f32_16x16x32_bf16 v[104:107], v[146:149], v[170:173], v[104:107]
	v_mfma_f32_16x16x32_bf16 v[100:103], v[154:157], v[170:173], v[100:103]
	v_mfma_f32_16x16x32_bf16 v[92:95], v[146:149], v[194:197], v[92:95]
	v_mfma_f32_16x16x32_bf16 v[84:87], v[154:157], v[194:197], v[84:87]
	v_mfma_f32_16x16x32_bf16 v[76:79], v[146:149], v[202:205], v[76:79]
	v_mfma_f32_16x16x32_bf16 v[68:71], v[154:157], v[202:205], v[68:71]
	v_mfma_f32_16x16x32_bf16 v[120:123], v[150:153], v[166:169], v[120:123]
	v_mfma_f32_16x16x32_bf16 v[116:119], v[158:161], v[166:169], v[116:119]
	v_mfma_f32_16x16x32_bf16 v[104:107], v[150:153], v[190:193], v[104:107]
	v_mfma_f32_16x16x32_bf16 v[100:103], v[158:161], v[190:193], v[100:103]
	v_mfma_f32_16x16x32_bf16 v[92:95], v[150:153], v[198:201], v[92:95]
	v_mfma_f32_16x16x32_bf16 v[84:87], v[158:161], v[198:201], v[84:87]
	v_mfma_f32_16x16x32_bf16 v[76:79], v[150:153], v[206:209], v[76:79]
	v_mfma_f32_16x16x32_bf16 v[68:71], v[158:161], v[206:209], v[68:71]
	s_barrier
	v_add_u32_e32 v0, s81, v139
	ds_read_b128 v[210:213], v0
	ds_read_b128 v[214:217], v0 offset:1024
	ds_read_b128 v[218:221], v0 offset:2048
	ds_read_b128 v[222:225], v0 offset:3072
	s_mov_b64 s[66:67], s[24:25]
	v_mov_b32_e32 v0, v135
	s_mov_b32 m0, s71
	s_nop 0
	global_load_lds_dwordx4 v0, s[66:67]
	v_mov_b32_e32 v0, v137
	s_mov_b32 m0, s84
	s_nop 0
	global_load_lds_dwordx4 v0, s[66:67]
	s_barrier
	s_waitcnt lgkmcnt(0)
	s_waitcnt lgkmcnt(0)
	v_mfma_f32_16x16x32_bf16 v[128:131], v[210:213], v[162:165], v[128:131]
	v_mfma_f32_16x16x32_bf16 v[124:127], v[218:221], v[162:165], v[124:127]
	v_mfma_f32_16x16x32_bf16 v[112:115], v[210:213], v[170:173], v[112:115]
	v_mfma_f32_16x16x32_bf16 v[108:111], v[218:221], v[170:173], v[108:111]
	v_mfma_f32_16x16x32_bf16 v[96:99], v[210:213], v[194:197], v[96:99]
	v_mfma_f32_16x16x32_bf16 v[88:91], v[218:221], v[194:197], v[88:91]
	v_mfma_f32_16x16x32_bf16 v[80:83], v[210:213], v[202:205], v[80:83]
	v_mfma_f32_16x16x32_bf16 v[72:75], v[218:221], v[202:205], v[72:75]
	v_mfma_f32_16x16x32_bf16 v[128:131], v[214:217], v[166:169], v[128:131]
	v_mfma_f32_16x16x32_bf16 v[124:127], v[222:225], v[166:169], v[124:127]
	v_mfma_f32_16x16x32_bf16 v[112:115], v[214:217], v[190:193], v[112:115]
	v_mfma_f32_16x16x32_bf16 v[108:111], v[222:225], v[190:193], v[108:111]
	v_mfma_f32_16x16x32_bf16 v[96:99], v[214:217], v[198:201], v[96:99]
	v_mfma_f32_16x16x32_bf16 v[88:91], v[222:225], v[198:201], v[88:91]
	v_mfma_f32_16x16x32_bf16 v[80:83], v[214:217], v[206:209], v[80:83]
	v_mfma_f32_16x16x32_bf16 v[72:75], v[222:225], v[206:209], v[72:75]
	s_cselect_b32 s85, s48, s58
	s_cselect_b32 s84, s49, s59
	s_add_u32 s66, s85, s64
	s_addc_u32 s67, s84, s45
	s_mov_b64 s[70:71], s[66:67]
	v_mov_b32_e32 v0, v134
	s_mov_b32 m0, s46
	s_barrier
	ds_read_b128 v[162:165], v141 offset:16384
	ds_read_b128 v[166:169], v141 offset:17408
	ds_read_b128 v[170:173], v141 offset:18432
	ds_read_b128 v[190:193], v141 offset:19456
	ds_read_b128 v[194:197], v141 offset:20480
	ds_read_b128 v[198:201], v141 offset:21504
	ds_read_b128 v[202:205], v141 offset:22528
	ds_read_b128 v[206:209], v141 offset:23552
	s_nop 0
	global_load_lds_dwordx4 v0, s[70:71]
	v_mov_b32_e32 v0, v136
	s_mov_b32 m0, s47
	s_nop 0
	global_load_lds_dwordx4 v0, s[70:71]
	s_barrier
	s_waitcnt lgkmcnt(0)
	s_waitcnt lgkmcnt(0)
	v_mfma_f32_16x16x32_bf16 v[56:59], v[146:149], v[162:165], v[56:59]
	v_mfma_f32_16x16x32_bf16 v[52:55], v[154:157], v[162:165], v[52:55]
	v_mfma_f32_16x16x32_bf16 v[40:43], v[146:149], v[170:173], v[40:43]
	v_mfma_f32_16x16x32_bf16 v[36:39], v[154:157], v[170:173], v[36:39]
	v_mfma_f32_16x16x32_bf16 v[24:27], v[146:149], v[194:197], v[24:27]
	v_mfma_f32_16x16x32_bf16 v[20:23], v[154:157], v[194:197], v[20:23]
	v_mfma_f32_16x16x32_bf16 v[12:15], v[146:149], v[202:205], v[12:15]
	v_mfma_f32_16x16x32_bf16 v[8:11], v[154:157], v[202:205], v[8:11]
	v_mfma_f32_16x16x32_bf16 v[56:59], v[150:153], v[166:169], v[56:59]
	v_mfma_f32_16x16x32_bf16 v[52:55], v[158:161], v[166:169], v[52:55]
	v_mfma_f32_16x16x32_bf16 v[40:43], v[150:153], v[190:193], v[40:43]
	v_mfma_f32_16x16x32_bf16 v[36:39], v[158:161], v[190:193], v[36:39]
	v_mfma_f32_16x16x32_bf16 v[24:27], v[150:153], v[198:201], v[24:27]
	v_mfma_f32_16x16x32_bf16 v[20:23], v[158:161], v[198:201], v[20:23]
	v_mfma_f32_16x16x32_bf16 v[12:15], v[150:153], v[206:209], v[12:15]
	v_mfma_f32_16x16x32_bf16 v[8:11], v[158:161], v[206:209], v[8:11]
	s_barrier
	s_add_u32 s70, s24, s6
	s_addc_u32 s71, s25, s7
	v_mov_b32_e32 v0, v135
	s_add_i32 s81, s81, s26
	s_mov_b32 m0, s81
	s_nop 0
	global_load_lds_dwordx4 v0, s[70:71]
	v_mov_b32_e32 v0, v137
	s_add_i32 m0, s81, 0x2000
	s_nop 0
	global_load_lds_dwordx4 v0, s[70:71]
	s_waitcnt vmcnt(6)
	s_barrier
	v_mfma_f32_16x16x32_bf16 v[64:67], v[210:213], v[162:165], v[64:67]
	v_mfma_f32_16x16x32_bf16 v[60:63], v[218:221], v[162:165], v[60:63]
	v_mfma_f32_16x16x32_bf16 v[48:51], v[210:213], v[170:173], v[48:51]
	v_mfma_f32_16x16x32_bf16 v[44:47], v[218:221], v[170:173], v[44:47]
	v_mfma_f32_16x16x32_bf16 v[32:35], v[210:213], v[194:197], v[32:35]
	v_mfma_f32_16x16x32_bf16 v[28:31], v[218:221], v[194:197], v[28:31]
	v_mfma_f32_16x16x32_bf16 v[16:19], v[210:213], v[202:205], v[16:19]
	v_mfma_f32_16x16x32_bf16 v[4:7], v[218:221], v[202:205], v[4:7]
	v_mfma_f32_16x16x32_bf16 v[64:67], v[214:217], v[166:169], v[64:67]
	v_mfma_f32_16x16x32_bf16 v[60:63], v[222:225], v[166:169], v[60:63]
	v_mfma_f32_16x16x32_bf16 v[48:51], v[214:217], v[190:193], v[48:51]
	v_mfma_f32_16x16x32_bf16 v[44:47], v[222:225], v[190:193], v[44:47]
	v_mfma_f32_16x16x32_bf16 v[32:35], v[214:217], v[198:201], v[32:35]
	v_mfma_f32_16x16x32_bf16 v[28:31], v[222:225], v[198:201], v[28:31]
	v_mfma_f32_16x16x32_bf16 v[16:19], v[214:217], v[206:209], v[16:19]
	v_mfma_f32_16x16x32_bf16 v[4:7], v[222:225], v[206:209], v[4:7]
	s_add_i32 s81, 0, 0x18000
	v_add_u32_e32 v0, s81, v139
	s_barrier
	ds_read_b128 v[146:149], v0
	ds_read_b128 v[150:153], v0 offset:1024
	ds_read_b128 v[154:157], v0 offset:2048
	ds_read_b128 v[158:161], v0 offset:3072
	s_add_u32 s70, s85, s0
	s_addc_u32 s71, s84, s1
	s_add_u32 s70, s70, s64
	s_addc_u32 s71, s71, s45
	v_mov_b32_e32 v0, v134
	s_mov_b32 m0, s51
	ds_read_b128 v[162:165], v141 offset:32768
	ds_read_b128 v[166:169], v141 offset:33792
	ds_read_b128 v[170:173], v141 offset:34816
	ds_read_b128 v[190:193], v141 offset:35840
	ds_read_b128 v[194:197], v141 offset:36864
	ds_read_b128 v[198:201], v141 offset:37888
	ds_read_b128 v[202:205], v141 offset:38912
	ds_read_b128 v[206:209], v141 offset:39936
	s_nop 0
	global_load_lds_dwordx4 v0, s[70:71]
	v_mov_b32_e32 v0, v136
	s_mov_b32 m0, s53
	s_nop 0
	global_load_lds_dwordx4 v0, s[70:71]
	s_waitcnt lgkmcnt(8)
	s_barrier
	s_waitcnt lgkmcnt(0)
	s_waitcnt lgkmcnt(0)
	v_mfma_f32_16x16x32_bf16 v[120:123], v[146:149], v[162:165], v[120:123]
	v_mfma_f32_16x16x32_bf16 v[116:119], v[154:157], v[162:165], v[116:119]
	v_mfma_f32_16x16x32_bf16 v[104:107], v[146:149], v[170:173], v[104:107]
	v_mfma_f32_16x16x32_bf16 v[100:103], v[154:157], v[170:173], v[100:103]
	v_mfma_f32_16x16x32_bf16 v[92:95], v[146:149], v[194:197], v[92:95]
	v_mfma_f32_16x16x32_bf16 v[84:87], v[154:157], v[194:197], v[84:87]
	v_mfma_f32_16x16x32_bf16 v[76:79], v[146:149], v[202:205], v[76:79]
	v_mfma_f32_16x16x32_bf16 v[68:71], v[154:157], v[202:205], v[68:71]
	v_mfma_f32_16x16x32_bf16 v[120:123], v[150:153], v[166:169], v[120:123]
	v_mfma_f32_16x16x32_bf16 v[116:119], v[158:161], v[166:169], v[116:119]
	v_mfma_f32_16x16x32_bf16 v[104:107], v[150:153], v[190:193], v[104:107]
	v_mfma_f32_16x16x32_bf16 v[100:103], v[158:161], v[190:193], v[100:103]
	v_mfma_f32_16x16x32_bf16 v[92:95], v[150:153], v[198:201], v[92:95]
	v_mfma_f32_16x16x32_bf16 v[84:87], v[158:161], v[198:201], v[84:87]
	v_mfma_f32_16x16x32_bf16 v[76:79], v[150:153], v[206:209], v[76:79]
	v_mfma_f32_16x16x32_bf16 v[68:71], v[158:161], v[206:209], v[68:71]
	s_barrier
	s_add_i32 s45, 0, 0x1c000
	s_add_u32 s24, s24, 0x80
	v_add_u32_e32 v0, s45, v139
	s_addc_u32 s25, s25, 0
	ds_read_b128 v[210:213], v0
	ds_read_b128 v[214:217], v0 offset:1024
	ds_read_b128 v[218:221], v0 offset:2048
	ds_read_b128 v[222:225], v0 offset:3072
	s_mov_b64 s[70:71], s[24:25]
	v_mov_b32_e32 v0, v135
	s_add_i32 s64, s81, s26
	s_mov_b32 m0, s64
	s_nop 0
	global_load_lds_dwordx4 v0, s[70:71]
	v_mov_b32_e32 v0, v137
	s_add_i32 m0, s64, 0x2000
	s_nop 0
	global_load_lds_dwordx4 v0, s[70:71]
	s_barrier
	s_waitcnt lgkmcnt(0)
	s_waitcnt lgkmcnt(0)
	v_mfma_f32_16x16x32_bf16 v[128:131], v[210:213], v[162:165], v[128:131]
	v_mfma_f32_16x16x32_bf16 v[124:127], v[218:221], v[162:165], v[124:127]
	v_mfma_f32_16x16x32_bf16 v[112:115], v[210:213], v[170:173], v[112:115]
	v_mfma_f32_16x16x32_bf16 v[108:111], v[218:221], v[170:173], v[108:111]
	v_mfma_f32_16x16x32_bf16 v[96:99], v[210:213], v[194:197], v[96:99]
	v_mfma_f32_16x16x32_bf16 v[88:91], v[218:221], v[194:197], v[88:91]
	v_mfma_f32_16x16x32_bf16 v[80:83], v[210:213], v[202:205], v[80:83]
	v_mfma_f32_16x16x32_bf16 v[72:75], v[218:221], v[202:205], v[72:75]
	v_mfma_f32_16x16x32_bf16 v[128:131], v[214:217], v[166:169], v[128:131]
	v_mfma_f32_16x16x32_bf16 v[124:127], v[222:225], v[166:169], v[124:127]
	v_mfma_f32_16x16x32_bf16 v[112:115], v[214:217], v[190:193], v[112:115]
	v_mfma_f32_16x16x32_bf16 v[108:111], v[222:225], v[190:193], v[108:111]
	v_mfma_f32_16x16x32_bf16 v[96:99], v[214:217], v[198:201], v[96:99]
	v_mfma_f32_16x16x32_bf16 v[88:91], v[222:225], v[198:201], v[88:91]
	v_mfma_f32_16x16x32_bf16 v[80:83], v[214:217], v[206:209], v[80:83]
	v_mfma_f32_16x16x32_bf16 v[72:75], v[222:225], v[206:209], v[72:75]
	s_add_u32 s66, s66, 0x80
	s_addc_u32 s67, s67, 0
	v_mov_b32_e32 v0, v134
	s_mov_b32 m0, s55
	s_barrier
	ds_read_b128 v[162:165], v141 offset:49152
	ds_read_b128 v[166:169], v141 offset:50176
	ds_read_b128 v[170:173], v141 offset:51200
	ds_read_b128 v[190:193], v141 offset:52224
	ds_read_b128 v[194:197], v141 offset:53248
	ds_read_b128 v[198:201], v141 offset:54272
	ds_read_b128 v[202:205], v141 offset:55296
	ds_read_b128 v[206:209], v141 offset:56320
	s_nop 0
	global_load_lds_dwordx4 v0, s[66:67]
	v_mov_b32_e32 v0, v136
	s_mov_b32 m0, s69
	s_nop 0
	global_load_lds_dwordx4 v0, s[66:67]
	s_barrier
	s_waitcnt lgkmcnt(0)
	s_waitcnt lgkmcnt(0)
	v_mfma_f32_16x16x32_bf16 v[56:59], v[146:149], v[162:165], v[56:59]
	v_mfma_f32_16x16x32_bf16 v[52:55], v[154:157], v[162:165], v[52:55]
	v_mfma_f32_16x16x32_bf16 v[40:43], v[146:149], v[170:173], v[40:43]
	v_mfma_f32_16x16x32_bf16 v[36:39], v[154:157], v[170:173], v[36:39]
	v_mfma_f32_16x16x32_bf16 v[24:27], v[146:149], v[194:197], v[24:27]
	v_mfma_f32_16x16x32_bf16 v[20:23], v[154:157], v[194:197], v[20:23]
	v_mfma_f32_16x16x32_bf16 v[12:15], v[146:149], v[202:205], v[12:15]
	v_mfma_f32_16x16x32_bf16 v[8:11], v[154:157], v[202:205], v[8:11]
	v_mfma_f32_16x16x32_bf16 v[56:59], v[150:153], v[166:169], v[56:59]
	v_mfma_f32_16x16x32_bf16 v[52:55], v[158:161], v[166:169], v[52:55]
	v_mfma_f32_16x16x32_bf16 v[40:43], v[150:153], v[190:193], v[40:43]
	v_mfma_f32_16x16x32_bf16 v[36:39], v[158:161], v[190:193], v[36:39]
	v_mfma_f32_16x16x32_bf16 v[24:27], v[150:153], v[198:201], v[24:27]
	v_mfma_f32_16x16x32_bf16 v[20:23], v[158:161], v[198:201], v[20:23]
	v_mfma_f32_16x16x32_bf16 v[12:15], v[150:153], v[206:209], v[12:15]
	v_mfma_f32_16x16x32_bf16 v[8:11], v[158:161], v[206:209], v[8:11]
	s_barrier
	s_add_u32 s24, s24, s6
	s_addc_u32 s25, s25, s7
	v_mov_b32_e32 v0, v135
	s_add_i32 s45, s45, s26
	s_mov_b32 m0, s45
	s_nop 0
	global_load_lds_dwordx4 v0, s[24:25]
	v_mov_b32_e32 v0, v137
	s_add_i32 m0, s45, 0x2000
	s_nop 0
	global_load_lds_dwordx4 v0, s[24:25]
	s_waitcnt vmcnt(6)
	s_barrier
	v_mfma_f32_16x16x32_bf16 v[64:67], v[210:213], v[162:165], v[64:67]
	v_mfma_f32_16x16x32_bf16 v[60:63], v[218:221], v[162:165], v[60:63]
	v_mfma_f32_16x16x32_bf16 v[48:51], v[210:213], v[170:173], v[48:51]
	v_mfma_f32_16x16x32_bf16 v[44:47], v[218:221], v[170:173], v[44:47]
	v_mfma_f32_16x16x32_bf16 v[32:35], v[210:213], v[194:197], v[32:35]
	v_mfma_f32_16x16x32_bf16 v[28:31], v[218:221], v[194:197], v[28:31]
	v_mfma_f32_16x16x32_bf16 v[16:19], v[210:213], v[202:205], v[16:19]
	v_mfma_f32_16x16x32_bf16 v[4:7], v[218:221], v[202:205], v[4:7]
	v_mfma_f32_16x16x32_bf16 v[64:67], v[214:217], v[166:169], v[64:67]
	v_mfma_f32_16x16x32_bf16 v[60:63], v[222:225], v[166:169], v[60:63]
	v_mfma_f32_16x16x32_bf16 v[48:51], v[214:217], v[190:193], v[48:51]
	v_mfma_f32_16x16x32_bf16 v[44:47], v[222:225], v[190:193], v[44:47]
	v_mfma_f32_16x16x32_bf16 v[32:35], v[214:217], v[198:201], v[32:35]
	v_mfma_f32_16x16x32_bf16 v[28:31], v[222:225], v[198:201], v[28:31]
	v_mfma_f32_16x16x32_bf16 v[16:19], v[214:217], v[206:209], v[16:19]
	v_mfma_f32_16x16x32_bf16 v[4:7], v[222:225], v[206:209], v[4:7]
	s_add_u32 s29, s29, 0x100
	s_addc_u32 s30, s30, 0
	s_cmp_lt_i32 s31, s54
	s_mov_b32 s24, s31
	s_barrier
	s_cbranch_scc1 .LBB0_371
	v_readlane_b32 s70, v254, 63
	v_readlane_b32 s71, v255, 0
	s_mul_i32 s81, s3, 24
	s_and_b64 vcc, exec, s[40:41]
	s_cbranch_vccz .LBB0_376
	s_branch .LBB0_377

; template <class Epi, class Sched>
; __device__ __forceinline__ void gemm_phase(LAS unsigned char* lds, const int K_, const Sched& S, const Epi& E, const int wave_) {
;     ...
;         if (Epi::NSTORE > 0 && hoisted) { PG8_BODY(true); t = 2; }
.LBB0_374:
	s_add_u32 s24, s56, 0x100
	s_addc_u32 s25, s57, 0
	s_and_b64 s[20:21], s[8:9], exec
	s_cselect_b32 s25, s43, s25
	s_cselect_b32 s24, s42, s24
	s_add_i32 s29, 0, 0x10000
	v_add_u32_e32 v0, s29, v139
	ds_read_b128 v[146:149], v0
	ds_read_b128 v[150:153], v0 offset:1024
	ds_read_b128 v[154:157], v0 offset:2048
	ds_read_b128 v[158:161], v0 offset:3072
	ds_read_b128 v[162:165], v141
	ds_read_b128 v[166:169], v141 offset:1024
	ds_read_b128 v[170:173], v141 offset:2048
	ds_read_b128 v[190:193], v141 offset:3072
	ds_read_b128 v[194:197], v141 offset:4096
	ds_read_b128 v[198:201], v141 offset:5120
	ds_read_b128 v[202:205], v141 offset:6144
	ds_read_b128 v[206:209], v141 offset:7168
	s_waitcnt lgkmcnt(8)
	s_barrier
	s_waitcnt lgkmcnt(0)
	s_waitcnt lgkmcnt(0)
	v_mfma_f32_16x16x32_bf16 v[120:123], v[146:149], v[162:165], v[120:123]
	v_mfma_f32_16x16x32_bf16 v[116:119], v[154:157], v[162:165], v[116:119]
	v_mfma_f32_16x16x32_bf16 v[104:107], v[146:149], v[170:173], v[104:107]
	v_mfma_f32_16x16x32_bf16 v[100:103], v[154:157], v[170:173], v[100:103]
	v_mfma_f32_16x16x32_bf16 v[92:95], v[146:149], v[194:197], v[92:95]
	v_mfma_f32_16x16x32_bf16 v[84:87], v[154:157], v[194:197], v[84:87]
	v_mfma_f32_16x16x32_bf16 v[76:79], v[146:149], v[202:205], v[76:79]
	v_mfma_f32_16x16x32_bf16 v[68:71], v[154:157], v[202:205], v[68:71]
	v_mfma_f32_16x16x32_bf16 v[120:123], v[150:153], v[166:169], v[120:123]
	v_mfma_f32_16x16x32_bf16 v[116:119], v[158:161], v[166:169], v[116:119]
	v_mfma_f32_16x16x32_bf16 v[104:107], v[150:153], v[190:193], v[104:107]
	v_mfma_f32_16x16x32_bf16 v[100:103], v[158:161], v[190:193], v[100:103]
	v_mfma_f32_16x16x32_bf16 v[92:95], v[150:153], v[198:201], v[92:95]
	v_mfma_f32_16x16x32_bf16 v[84:87], v[158:161], v[198:201], v[84:87]
	v_mfma_f32_16x16x32_bf16 v[76:79], v[150:153], v[206:209], v[76:79]
	v_mfma_f32_16x16x32_bf16 v[68:71], v[158:161], v[206:209], v[68:71]
	s_barrier
	s_add_i32 s30, 0, 0x14000
	v_add_u32_e32 v0, s30, v139
	ds_read_b128 v[210:213], v0
	ds_read_b128 v[214:217], v0 offset:1024
	ds_read_b128 v[218:221], v0 offset:2048
	ds_read_b128 v[222:225], v0 offset:3072
	s_mov_b64 s[20:21], s[24:25]
	v_mov_b32_e32 v0, v135
	s_add_i32 s29, s29, s26
	s_mov_b32 m0, s29
	s_nop 0
	global_load_lds_dwordx4 v0, s[20:21]
	v_mov_b32_e32 v0, v137
	s_add_i32 m0, s29, 0x2000
	s_nop 0
	global_load_lds_dwordx4 v0, s[20:21]
	s_barrier
	s_waitcnt lgkmcnt(0)
	s_waitcnt lgkmcnt(0)
	v_mfma_f32_16x16x32_bf16 v[128:131], v[210:213], v[162:165], v[128:131]
	v_mfma_f32_16x16x32_bf16 v[124:127], v[218:221], v[162:165], v[124:127]
	v_mfma_f32_16x16x32_bf16 v[112:115], v[210:213], v[170:173], v[112:115]
	v_mfma_f32_16x16x32_bf16 v[108:111], v[218:221], v[170:173], v[108:111]
	v_mfma_f32_16x16x32_bf16 v[96:99], v[210:213], v[194:197], v[96:99]
	v_mfma_f32_16x16x32_bf16 v[88:91], v[218:221], v[194:197], v[88:91]
	v_mfma_f32_16x16x32_bf16 v[80:83], v[210:213], v[202:205], v[80:83]
	v_mfma_f32_16x16x32_bf16 v[72:75], v[218:221], v[202:205], v[72:75]
	v_mfma_f32_16x16x32_bf16 v[128:131], v[214:217], v[166:169], v[128:131]
	v_mfma_f32_16x16x32_bf16 v[124:127], v[222:225], v[166:169], v[124:127]
	v_mfma_f32_16x16x32_bf16 v[112:115], v[214:217], v[190:193], v[112:115]
	v_mfma_f32_16x16x32_bf16 v[108:111], v[222:225], v[190:193], v[108:111]
	v_mfma_f32_16x16x32_bf16 v[96:99], v[214:217], v[198:201], v[96:99]
	v_mfma_f32_16x16x32_bf16 v[88:91], v[222:225], v[198:201], v[88:91]
	v_mfma_f32_16x16x32_bf16 v[80:83], v[214:217], v[206:209], v[80:83]
	v_mfma_f32_16x16x32_bf16 v[72:75], v[222:225], v[206:209], v[72:75]
	s_and_b64 s[20:21], s[8:9], exec
	s_cselect_b32 s31, s48, s58
	s_cselect_b32 s29, s49, s59
	s_add_u32 s66, s31, s75
	s_addc_u32 s67, s29, 0
	s_mov_b64 s[20:21], s[66:67]
	v_mov_b32_e32 v0, v134
	s_mov_b32 m0, s46
	s_barrier
	ds_read_b128 v[162:165], v141 offset:16384
	ds_read_b128 v[166:169], v141 offset:17408
	ds_read_b128 v[170:173], v141 offset:18432
	ds_read_b128 v[190:193], v141 offset:19456
	ds_read_b128 v[194:197], v141 offset:20480
	ds_read_b128 v[198:201], v141 offset:21504
	ds_read_b128 v[202:205], v141 offset:22528
	ds_read_b128 v[206:209], v141 offset:23552
	s_nop 0
	global_load_lds_dwordx4 v0, s[20:21]
	v_mov_b32_e32 v0, v136
	s_mov_b32 m0, s47
	s_nop 0
	global_load_lds_dwordx4 v0, s[20:21]
	s_barrier
	s_waitcnt lgkmcnt(0)
	s_waitcnt lgkmcnt(0)
	v_mfma_f32_16x16x32_bf16 v[56:59], v[146:149], v[162:165], v[56:59]
	v_mfma_f32_16x16x32_bf16 v[52:55], v[154:157], v[162:165], v[52:55]
	v_mfma_f32_16x16x32_bf16 v[40:43], v[146:149], v[170:173], v[40:43]
	v_mfma_f32_16x16x32_bf16 v[36:39], v[154:157], v[170:173], v[36:39]
	v_mfma_f32_16x16x32_bf16 v[24:27], v[146:149], v[194:197], v[24:27]
	v_mfma_f32_16x16x32_bf16 v[20:23], v[154:157], v[194:197], v[20:23]
	v_mfma_f32_16x16x32_bf16 v[12:15], v[146:149], v[202:205], v[12:15]
	v_mfma_f32_16x16x32_bf16 v[8:11], v[154:157], v[202:205], v[8:11]
	v_mfma_f32_16x16x32_bf16 v[56:59], v[150:153], v[166:169], v[56:59]
	v_mfma_f32_16x16x32_bf16 v[52:55], v[158:161], v[166:169], v[52:55]
	v_mfma_f32_16x16x32_bf16 v[40:43], v[150:153], v[190:193], v[40:43]
	v_mfma_f32_16x16x32_bf16 v[36:39], v[158:161], v[190:193], v[36:39]
	v_mfma_f32_16x16x32_bf16 v[24:27], v[150:153], v[198:201], v[24:27]
	v_mfma_f32_16x16x32_bf16 v[20:23], v[158:161], v[198:201], v[20:23]
	v_mfma_f32_16x16x32_bf16 v[12:15], v[150:153], v[206:209], v[12:15]
	v_mfma_f32_16x16x32_bf16 v[8:11], v[158:161], v[206:209], v[8:11]
	s_barrier
	s_add_u32 s20, s24, s6
	s_addc_u32 s21, s25, s7
	v_mov_b32_e32 v0, v135
	s_add_i32 s30, s30, s26
	s_mov_b32 m0, s30
	s_nop 0
	global_load_lds_dwordx4 v0, s[20:21]
	v_mov_b32_e32 v0, v137
	s_add_i32 m0, s30, 0x2000
	s_nop 0
	global_load_lds_dwordx4 v0, s[20:21]
	s_waitcnt vmcnt(22)
	s_barrier
	v_mfma_f32_16x16x32_bf16 v[64:67], v[210:213], v[162:165], v[64:67]
	v_mfma_f32_16x16x32_bf16 v[60:63], v[218:221], v[162:165], v[60:63]
	v_mfma_f32_16x16x32_bf16 v[48:51], v[210:213], v[170:173], v[48:51]
	v_mfma_f32_16x16x32_bf16 v[44:47], v[218:221], v[170:173], v[44:47]
	v_mfma_f32_16x16x32_bf16 v[32:35], v[210:213], v[194:197], v[32:35]
	v_mfma_f32_16x16x32_bf16 v[28:31], v[218:221], v[194:197], v[28:31]
	v_mfma_f32_16x16x32_bf16 v[16:19], v[210:213], v[202:205], v[16:19]
	v_mfma_f32_16x16x32_bf16 v[4:7], v[218:221], v[202:205], v[4:7]
	v_mfma_f32_16x16x32_bf16 v[64:67], v[214:217], v[166:169], v[64:67]
	v_mfma_f32_16x16x32_bf16 v[60:63], v[222:225], v[166:169], v[60:63]
	v_mfma_f32_16x16x32_bf16 v[48:51], v[214:217], v[190:193], v[48:51]
	v_mfma_f32_16x16x32_bf16 v[44:47], v[222:225], v[190:193], v[44:47]
	v_mfma_f32_16x16x32_bf16 v[32:35], v[214:217], v[198:201], v[32:35]
	v_mfma_f32_16x16x32_bf16 v[28:31], v[222:225], v[198:201], v[28:31]
	v_mfma_f32_16x16x32_bf16 v[16:19], v[214:217], v[206:209], v[16:19]
	v_mfma_f32_16x16x32_bf16 v[4:7], v[222:225], v[206:209], v[4:7]
	s_add_i32 s30, 0, 0x18000
	v_add_u32_e32 v0, s30, v139
	s_barrier
	ds_read_b128 v[146:149], v0
	ds_read_b128 v[150:153], v0 offset:1024
	ds_read_b128 v[154:157], v0 offset:2048
	ds_read_b128 v[158:161], v0 offset:3072
	s_add_u32 s20, s31, s0
	s_addc_u32 s21, s29, s1
	s_add_u32 s20, s20, s75
	s_addc_u32 s21, s21, 0
	v_mov_b32_e32 v0, v134
	s_mov_b32 m0, s51
	ds_read_b128 v[162:165], v141 offset:32768
	ds_read_b128 v[166:169], v141 offset:33792
	ds_read_b128 v[170:173], v141 offset:34816
	ds_read_b128 v[190:193], v141 offset:35840
	ds_read_b128 v[194:197], v141 offset:36864
	ds_read_b128 v[198:201], v141 offset:37888
	ds_read_b128 v[202:205], v141 offset:38912
	ds_read_b128 v[206:209], v141 offset:39936
	s_nop 0
	global_load_lds_dwordx4 v0, s[20:21]
	v_mov_b32_e32 v0, v136
	s_mov_b32 m0, s53
	s_nop 0
	global_load_lds_dwordx4 v0, s[20:21]
	s_waitcnt lgkmcnt(8)
	s_barrier
	s_waitcnt lgkmcnt(0)
	s_waitcnt lgkmcnt(0)
	v_mfma_f32_16x16x32_bf16 v[120:123], v[146:149], v[162:165], v[120:123]
	v_mfma_f32_16x16x32_bf16 v[116:119], v[154:157], v[162:165], v[116:119]
	v_mfma_f32_16x16x32_bf16 v[104:107], v[146:149], v[170:173], v[104:107]
	v_mfma_f32_16x16x32_bf16 v[100:103], v[154:157], v[170:173], v[100:103]
	v_mfma_f32_16x16x32_bf16 v[92:95], v[146:149], v[194:197], v[92:95]
	v_mfma_f32_16x16x32_bf16 v[84:87], v[154:157], v[194:197], v[84:87]
	v_mfma_f32_16x16x32_bf16 v[76:79], v[146:149], v[202:205], v[76:79]
	v_mfma_f32_16x16x32_bf16 v[68:71], v[154:157], v[202:205], v[68:71]
	v_mfma_f32_16x16x32_bf16 v[120:123], v[150:153], v[166:169], v[120:123]
	v_mfma_f32_16x16x32_bf16 v[116:119], v[158:161], v[166:169], v[116:119]
	v_mfma_f32_16x16x32_bf16 v[104:107], v[150:153], v[190:193], v[104:107]
	v_mfma_f32_16x16x32_bf16 v[100:103], v[158:161], v[190:193], v[100:103]
	v_mfma_f32_16x16x32_bf16 v[92:95], v[150:153], v[198:201], v[92:95]
	v_mfma_f32_16x16x32_bf16 v[84:87], v[158:161], v[198:201], v[84:87]
	v_mfma_f32_16x16x32_bf16 v[76:79], v[150:153], v[206:209], v[76:79]
	v_mfma_f32_16x16x32_bf16 v[68:71], v[158:161], v[206:209], v[68:71]
	s_barrier
	s_add_i32 s29, 0, 0x1c000
	s_add_u32 s20, s24, 0x80
	v_add_u32_e32 v0, s29, v139
	s_addc_u32 s21, s25, 0
	ds_read_b128 v[210:213], v0
	ds_read_b128 v[214:217], v0 offset:1024
	ds_read_b128 v[218:221], v0 offset:2048
	ds_read_b128 v[222:225], v0 offset:3072
	s_mov_b64 s[24:25], s[20:21]
	v_mov_b32_e32 v0, v135
	s_add_i32 s30, s30, s26
	s_mov_b32 m0, s30
	s_nop 0
	global_load_lds_dwordx4 v0, s[24:25]
	v_mov_b32_e32 v0, v137
	s_add_i32 m0, s30, 0x2000
	s_nop 0
	global_load_lds_dwordx4 v0, s[24:25]
	s_barrier
; template <class Epi, class Sched>
; __device__ __forceinline__ void gemm_phase(LAS unsigned char* lds, const int K_, const Sched& S, const Epi& E, const int wave_) {
;     ...
;         int t = 0;
;         if (Epi::NSTORE > 0 && hoisted) { PG8_BODY(true); t = 2; }
;         for (; t < nt; t += 2) { PG8_BODY(false); }
	s_waitcnt lgkmcnt(0)
	s_waitcnt lgkmcnt(0)
	v_mfma_f32_16x16x32_bf16 v[128:131], v[210:213], v[162:165], v[128:131]
	v_mfma_f32_16x16x32_bf16 v[124:127], v[218:221], v[162:165], v[124:127]
	v_mfma_f32_16x16x32_bf16 v[112:115], v[210:213], v[170:173], v[112:115]
	v_mfma_f32_16x16x32_bf16 v[108:111], v[218:221], v[170:173], v[108:111]
	v_mfma_f32_16x16x32_bf16 v[96:99], v[210:213], v[194:197], v[96:99]
	v_mfma_f32_16x16x32_bf16 v[88:91], v[218:221], v[194:197], v[88:91]
	v_mfma_f32_16x16x32_bf16 v[80:83], v[210:213], v[202:205], v[80:83]
	v_mfma_f32_16x16x32_bf16 v[72:75], v[218:221], v[202:205], v[72:75]
	v_mfma_f32_16x16x32_bf16 v[128:131], v[214:217], v[166:169], v[128:131]
	v_mfma_f32_16x16x32_bf16 v[124:127], v[222:225], v[166:169], v[124:127]
	v_mfma_f32_16x16x32_bf16 v[112:115], v[214:217], v[190:193], v[112:115]
	v_mfma_f32_16x16x32_bf16 v[108:111], v[222:225], v[190:193], v[108:111]
	v_mfma_f32_16x16x32_bf16 v[96:99], v[214:217], v[198:201], v[96:99]
	v_mfma_f32_16x16x32_bf16 v[88:91], v[222:225], v[198:201], v[88:91]
	v_mfma_f32_16x16x32_bf16 v[80:83], v[214:217], v[206:209], v[80:83]
	v_mfma_f32_16x16x32_bf16 v[72:75], v[222:225], v[206:209], v[72:75]
	s_add_u32 s24, s66, 0x80
	s_addc_u32 s25, s67, 0
	v_mov_b32_e32 v0, v134
	s_mov_b32 m0, s55
	s_barrier
	ds_read_b128 v[162:165], v141 offset:49152
	ds_read_b128 v[166:169], v141 offset:50176
	ds_read_b128 v[170:173], v141 offset:51200
	ds_read_b128 v[190:193], v141 offset:52224
	ds_read_b128 v[194:197], v141 offset:53248
	ds_read_b128 v[198:201], v141 offset:54272
	ds_read_b128 v[202:205], v141 offset:55296
	ds_read_b128 v[206:209], v141 offset:56320
	s_nop 0
	global_load_lds_dwordx4 v0, s[24:25]
	v_mov_b32_e32 v0, v136
	s_mov_b32 m0, s69
	s_nop 0
	global_load_lds_dwordx4 v0, s[24:25]
	s_barrier
	s_waitcnt lgkmcnt(0)
	s_waitcnt lgkmcnt(0)
	v_mfma_f32_16x16x32_bf16 v[56:59], v[146:149], v[162:165], v[56:59]
	v_mfma_f32_16x16x32_bf16 v[52:55], v[154:157], v[162:165], v[52:55]
	v_mfma_f32_16x16x32_bf16 v[40:43], v[146:149], v[170:173], v[40:43]
	v_mfma_f32_16x16x32_bf16 v[36:39], v[154:157], v[170:173], v[36:39]
	v_mfma_f32_16x16x32_bf16 v[24:27], v[146:149], v[194:197], v[24:27]
	v_mfma_f32_16x16x32_bf16 v[20:23], v[154:157], v[194:197], v[20:23]
	v_mfma_f32_16x16x32_bf16 v[12:15], v[146:149], v[202:205], v[12:15]
	v_mfma_f32_16x16x32_bf16 v[8:11], v[154:157], v[202:205], v[8:11]
	v_mfma_f32_16x16x32_bf16 v[56:59], v[150:153], v[166:169], v[56:59]
	v_mfma_f32_16x16x32_bf16 v[52:55], v[158:161], v[166:169], v[52:55]
	v_mfma_f32_16x16x32_bf16 v[40:43], v[150:153], v[190:193], v[40:43]
	v_mfma_f32_16x16x32_bf16 v[36:39], v[158:161], v[190:193], v[36:39]
	v_mfma_f32_16x16x32_bf16 v[24:27], v[150:153], v[198:201], v[24:27]
	v_mfma_f32_16x16x32_bf16 v[20:23], v[158:161], v[198:201], v[20:23]
	v_mfma_f32_16x16x32_bf16 v[12:15], v[150:153], v[206:209], v[12:15]
	v_mfma_f32_16x16x32_bf16 v[8:11], v[158:161], v[206:209], v[8:11]
	s_barrier
	s_add_u32 s20, s20, s6
	s_addc_u32 s21, s21, s7
	v_mov_b32_e32 v0, v135
	s_add_i32 s24, s29, s26
	s_mov_b32 m0, s24
	s_nop 0
	global_load_lds_dwordx4 v0, s[20:21]
	v_mov_b32_e32 v0, v137
	s_add_i32 m0, s24, 0x2000
	s_nop 0
	global_load_lds_dwordx4 v0, s[20:21]
	s_waitcnt vmcnt(6)
	s_barrier
	v_mfma_f32_16x16x32_bf16 v[64:67], v[210:213], v[162:165], v[64:67]
	v_mfma_f32_16x16x32_bf16 v[60:63], v[218:221], v[162:165], v[60:63]
	v_mfma_f32_16x16x32_bf16 v[48:51], v[210:213], v[170:173], v[48:51]
	v_mfma_f32_16x16x32_bf16 v[44:47], v[218:221], v[170:173], v[44:47]
	v_mfma_f32_16x16x32_bf16 v[32:35], v[210:213], v[194:197], v[32:35]
	v_mfma_f32_16x16x32_bf16 v[28:31], v[218:221], v[194:197], v[28:31]
	v_mfma_f32_16x16x32_bf16 v[16:19], v[210:213], v[202:205], v[16:19]
	v_mfma_f32_16x16x32_bf16 v[4:7], v[218:221], v[202:205], v[4:7]
	v_mfma_f32_16x16x32_bf16 v[64:67], v[214:217], v[166:169], v[64:67]
	v_mfma_f32_16x16x32_bf16 v[60:63], v[222:225], v[166:169], v[60:63]
	v_mfma_f32_16x16x32_bf16 v[48:51], v[214:217], v[190:193], v[48:51]
	v_mfma_f32_16x16x32_bf16 v[44:47], v[222:225], v[190:193], v[44:47]
	v_mfma_f32_16x16x32_bf16 v[32:35], v[214:217], v[198:201], v[32:35]
	v_mfma_f32_16x16x32_bf16 v[28:31], v[222:225], v[198:201], v[28:31]
	v_mfma_f32_16x16x32_bf16 v[16:19], v[214:217], v[206:209], v[16:19]
	v_mfma_f32_16x16x32_bf16 v[4:7], v[222:225], v[206:209], v[4:7]
	s_mov_b32 s24, 2
	s_barrier
	s_cmp_ge_i32 s24, s54
	s_cbranch_scc0 .LBB0_370

; template <class Epi, class Sched>
; __device__ __forceinline__ void gemm_phase(LAS unsigned char* lds, const int K_, const Sched& S, const Epi& E, const int wave_) {
;     ...
;         int t = 0;
;         if (Epi::NSTORE > 0 && hoisted) { PG8_BODY(true); t = 2; }
;         for (; t < nt; t += 2) { PG8_BODY(false); }
.LBB0_1242:
	s_add_i32 s51, s64, 2
	s_add_u32 s66, s56, s24
	s_addc_u32 s67, s57, s25
	s_add_i32 s86, 0, 0x10000
	v_add_u32_e32 v0, s86, v163
	s_add_u32 s84, s21, s24
	ds_read_b128 v[132:135], v0
	ds_read_b128 v[136:139], v0 offset:1024
	ds_read_b128 v[140:143], v0 offset:2048
	ds_read_b128 v[146:149], v0 offset:3072
	s_addc_u32 s85, s49, s25
	s_add_u32 s84, s84, 0xffffff80
	s_addc_u32 s85, s85, -1
	s_add_i32 vcc_hi, s86, s17
	s_add_i32 m0, s30, 0xc000
	s_add_i32 s87, s30, 0xe000
	s_add_i32 vcc_lo, 0, 0x14000
	s_add_i32 s89, vcc_hi, 0x2000
	s_cmp_eq_u32 s79, s64
	s_cselect_b32 s64, 0, s25
	s_cselect_b32 s67, s43, s67
	s_cselect_b32 s66, s42, s66
	s_cselect_b32 s14, 0, s24
	v_mov_b32_e32 v0, v160
	ds_read_b128 v[150:153], v165
	ds_read_b128 v[154:157], v165 offset:1024
	ds_read_b128 v[166:169], v165 offset:2048
	ds_read_b128 v[170:173], v165 offset:3072
	ds_read_b128 v[190:193], v165 offset:4096
	ds_read_b128 v[194:197], v165 offset:5120
	ds_read_b128 v[198:201], v165 offset:6144
	ds_read_b128 v[202:205], v165 offset:7168
	s_nop 0
	global_load_lds_dwordx4 v0, s[84:85]
	v_mov_b32_e32 v0, v161
	s_mov_b32 m0, s87
	s_nop 0
	global_load_lds_dwordx4 v0, s[84:85]
	s_waitcnt lgkmcnt(8)
	s_barrier
	s_waitcnt lgkmcnt(0)
	s_waitcnt lgkmcnt(0)
	v_mfma_f32_16x16x32_bf16 v[128:131], v[132:135], v[150:153], v[128:131]
	v_mfma_f32_16x16x32_bf16 v[96:99], v[140:143], v[150:153], v[96:99]
	v_mfma_f32_16x16x32_bf16 v[120:123], v[132:135], v[166:169], v[120:123]
	v_mfma_f32_16x16x32_bf16 v[88:91], v[140:143], v[166:169], v[88:91]
	v_mfma_f32_16x16x32_bf16 v[112:115], v[132:135], v[190:193], v[112:115]
	v_mfma_f32_16x16x32_bf16 v[80:83], v[140:143], v[190:193], v[80:83]
	v_mfma_f32_16x16x32_bf16 v[104:107], v[132:135], v[198:201], v[104:107]
	v_mfma_f32_16x16x32_bf16 v[72:75], v[140:143], v[198:201], v[72:75]
	v_mfma_f32_16x16x32_bf16 v[128:131], v[136:139], v[154:157], v[128:131]
	v_mfma_f32_16x16x32_bf16 v[96:99], v[146:149], v[154:157], v[96:99]
	v_mfma_f32_16x16x32_bf16 v[120:123], v[136:139], v[170:173], v[120:123]
	v_mfma_f32_16x16x32_bf16 v[88:91], v[146:149], v[170:173], v[88:91]
	v_mfma_f32_16x16x32_bf16 v[112:115], v[136:139], v[194:197], v[112:115]
	v_mfma_f32_16x16x32_bf16 v[80:83], v[146:149], v[194:197], v[80:83]
	v_mfma_f32_16x16x32_bf16 v[104:107], v[136:139], v[202:205], v[104:107]
	v_mfma_f32_16x16x32_bf16 v[72:75], v[146:149], v[202:205], v[72:75]
	s_barrier
	v_add_u32_e32 v0, vcc_lo, v163
	ds_read_b128 v[206:209], v0
	ds_read_b128 v[210:213], v0 offset:1024
	ds_read_b128 v[214:217], v0 offset:2048
	ds_read_b128 v[218:221], v0 offset:3072
	s_mov_b64 s[84:85], s[66:67]
	v_mov_b32_e32 v0, v160
	s_mov_b32 m0, vcc_hi
	s_nop 0
	global_load_lds_dwordx4 v0, s[84:85]
	v_mov_b32_e32 v0, v161
	s_mov_b32 m0, s89
	s_nop 0
	global_load_lds_dwordx4 v0, s[84:85]
	s_barrier
	s_waitcnt lgkmcnt(0)
	s_waitcnt lgkmcnt(0)
	v_mfma_f32_16x16x32_bf16 v[64:67], v[206:209], v[150:153], v[64:67]
	v_mfma_f32_16x16x32_bf16 v[32:35], v[214:217], v[150:153], v[32:35]
	v_mfma_f32_16x16x32_bf16 v[56:59], v[206:209], v[166:169], v[56:59]
	v_mfma_f32_16x16x32_bf16 v[24:27], v[214:217], v[166:169], v[24:27]
	v_mfma_f32_16x16x32_bf16 v[48:51], v[206:209], v[190:193], v[48:51]
	v_mfma_f32_16x16x32_bf16 v[16:19], v[214:217], v[190:193], v[16:19]
	v_mfma_f32_16x16x32_bf16 v[40:43], v[206:209], v[198:201], v[40:43]
	v_mfma_f32_16x16x32_bf16 v[8:11], v[214:217], v[198:201], v[8:11]
	v_mfma_f32_16x16x32_bf16 v[64:67], v[210:213], v[154:157], v[64:67]
	v_mfma_f32_16x16x32_bf16 v[32:35], v[218:221], v[154:157], v[32:35]
	v_mfma_f32_16x16x32_bf16 v[56:59], v[210:213], v[170:173], v[56:59]
	v_mfma_f32_16x16x32_bf16 v[24:27], v[218:221], v[170:173], v[24:27]
	v_mfma_f32_16x16x32_bf16 v[48:51], v[210:213], v[194:197], v[48:51]
	v_mfma_f32_16x16x32_bf16 v[16:19], v[218:221], v[194:197], v[16:19]
	v_mfma_f32_16x16x32_bf16 v[40:43], v[210:213], v[202:205], v[40:43]
	v_mfma_f32_16x16x32_bf16 v[8:11], v[218:221], v[202:205], v[8:11]
	s_cselect_b32 s89, s52, s58
	s_cselect_b32 s15, s53, s59
	s_add_u32 s84, s89, s14
	s_addc_u32 s85, s15, s64
	s_mov_b64 s[86:87], s[84:85]
	v_mov_b32_e32 v0, v160
	s_mov_b32 m0, s30
	s_barrier
	ds_read_b128 v[150:153], v165 offset:16384
	ds_read_b128 v[154:157], v165 offset:17408
	ds_read_b128 v[166:169], v165 offset:18432
	ds_read_b128 v[170:173], v165 offset:19456
	ds_read_b128 v[190:193], v165 offset:20480
	ds_read_b128 v[194:197], v165 offset:21504
	ds_read_b128 v[198:201], v165 offset:22528
	ds_read_b128 v[202:205], v165 offset:23552
	s_nop 0
	global_load_lds_dwordx4 v0, s[86:87]
	v_mov_b32_e32 v0, v161
	s_mov_b32 m0, s31
	s_nop 0
	global_load_lds_dwordx4 v0, s[86:87]
	s_barrier
	s_waitcnt lgkmcnt(0)
	s_waitcnt lgkmcnt(0)
	v_mfma_f32_16x16x32_bf16 v[124:127], v[132:135], v[150:153], v[124:127]
	v_mfma_f32_16x16x32_bf16 v[92:95], v[140:143], v[150:153], v[92:95]
	v_mfma_f32_16x16x32_bf16 v[116:119], v[132:135], v[166:169], v[116:119]
	v_mfma_f32_16x16x32_bf16 v[84:87], v[140:143], v[166:169], v[84:87]
	v_mfma_f32_16x16x32_bf16 v[108:111], v[132:135], v[190:193], v[108:111]
	v_mfma_f32_16x16x32_bf16 v[76:79], v[140:143], v[190:193], v[76:79]
	v_mfma_f32_16x16x32_bf16 v[100:103], v[132:135], v[198:201], v[100:103]
	v_mfma_f32_16x16x32_bf16 v[68:71], v[140:143], v[198:201], v[68:71]
	v_mfma_f32_16x16x32_bf16 v[124:127], v[136:139], v[154:157], v[124:127]
	v_mfma_f32_16x16x32_bf16 v[92:95], v[146:149], v[154:157], v[92:95]
	v_mfma_f32_16x16x32_bf16 v[116:119], v[136:139], v[170:173], v[116:119]
	v_mfma_f32_16x16x32_bf16 v[84:87], v[146:149], v[170:173], v[84:87]
	v_mfma_f32_16x16x32_bf16 v[108:111], v[136:139], v[194:197], v[108:111]
	v_mfma_f32_16x16x32_bf16 v[76:79], v[146:149], v[194:197], v[76:79]
	v_mfma_f32_16x16x32_bf16 v[100:103], v[136:139], v[202:205], v[100:103]
	v_mfma_f32_16x16x32_bf16 v[68:71], v[146:149], v[202:205], v[68:71]
	s_barrier
	s_add_u32 s86, s66, s44
	s_addc_u32 s87, s67, s45
	v_mov_b32_e32 v0, v160
	s_add_i32 vcc_lo, vcc_lo, s17
	s_mov_b32 m0, vcc_lo
	s_nop 0
	global_load_lds_dwordx4 v0, s[86:87]
	v_mov_b32_e32 v0, v161
	s_add_i32 m0, vcc_lo, 0x2000
	s_nop 0
	global_load_lds_dwordx4 v0, s[86:87]
	s_waitcnt vmcnt(6)
	s_barrier
	v_mfma_f32_16x16x32_bf16 v[60:63], v[206:209], v[150:153], v[60:63]
	v_mfma_f32_16x16x32_bf16 v[28:31], v[214:217], v[150:153], v[28:31]
	v_mfma_f32_16x16x32_bf16 v[52:55], v[206:209], v[166:169], v[52:55]
	v_mfma_f32_16x16x32_bf16 v[20:23], v[214:217], v[166:169], v[20:23]
	v_mfma_f32_16x16x32_bf16 v[44:47], v[206:209], v[190:193], v[44:47]
	v_mfma_f32_16x16x32_bf16 v[12:15], v[214:217], v[190:193], v[12:15]
	v_mfma_f32_16x16x32_bf16 v[36:39], v[206:209], v[198:201], v[36:39]
	v_mfma_f32_16x16x32_bf16 v[4:7], v[214:217], v[198:201], v[4:7]
	v_mfma_f32_16x16x32_bf16 v[60:63], v[210:213], v[154:157], v[60:63]
	v_mfma_f32_16x16x32_bf16 v[28:31], v[218:221], v[154:157], v[28:31]
	v_mfma_f32_16x16x32_bf16 v[52:55], v[210:213], v[170:173], v[52:55]
	v_mfma_f32_16x16x32_bf16 v[20:23], v[218:221], v[170:173], v[20:23]
	v_mfma_f32_16x16x32_bf16 v[44:47], v[210:213], v[194:197], v[44:47]
	v_mfma_f32_16x16x32_bf16 v[12:15], v[218:221], v[194:197], v[12:15]
	v_mfma_f32_16x16x32_bf16 v[36:39], v[210:213], v[202:205], v[36:39]
	v_mfma_f32_16x16x32_bf16 v[4:7], v[218:221], v[202:205], v[4:7]
	s_add_i32 vcc_lo, 0, 0x18000
	v_add_u32_e32 v0, vcc_lo, v163
	s_barrier
	ds_read_b128 v[132:135], v0
	ds_read_b128 v[136:139], v0 offset:1024
	ds_read_b128 v[140:143], v0 offset:2048
	ds_read_b128 v[146:149], v0 offset:3072
	s_add_u32 s86, s89, s44
	s_addc_u32 s15, s15, s45
	s_add_u32 s86, s86, s14
	s_addc_u32 s87, s15, s64
	v_mov_b32_e32 v0, v160
	s_mov_b32 m0, s55
	ds_read_b128 v[150:153], v165 offset:32768
	ds_read_b128 v[154:157], v165 offset:33792
	ds_read_b128 v[166:169], v165 offset:34816
	ds_read_b128 v[170:173], v165 offset:35840
	ds_read_b128 v[190:193], v165 offset:36864
	ds_read_b128 v[194:197], v165 offset:37888
	ds_read_b128 v[198:201], v165 offset:38912
	ds_read_b128 v[202:205], v165 offset:39936
	s_nop 0
	global_load_lds_dwordx4 v0, s[86:87]
	v_mov_b32_e32 v0, v161
	s_mov_b32 m0, s69
	s_nop 0
	global_load_lds_dwordx4 v0, s[86:87]
	s_waitcnt lgkmcnt(8)
	s_barrier
	s_waitcnt lgkmcnt(0)
	s_waitcnt lgkmcnt(0)
	v_mfma_f32_16x16x32_bf16 v[128:131], v[132:135], v[150:153], v[128:131]
	v_mfma_f32_16x16x32_bf16 v[96:99], v[140:143], v[150:153], v[96:99]
	v_mfma_f32_16x16x32_bf16 v[120:123], v[132:135], v[166:169], v[120:123]
	v_mfma_f32_16x16x32_bf16 v[88:91], v[140:143], v[166:169], v[88:91]
	v_mfma_f32_16x16x32_bf16 v[112:115], v[132:135], v[190:193], v[112:115]
	v_mfma_f32_16x16x32_bf16 v[80:83], v[140:143], v[190:193], v[80:83]
	v_mfma_f32_16x16x32_bf16 v[104:107], v[132:135], v[198:201], v[104:107]
	v_mfma_f32_16x16x32_bf16 v[72:75], v[140:143], v[198:201], v[72:75]
	v_mfma_f32_16x16x32_bf16 v[128:131], v[136:139], v[154:157], v[128:131]
	v_mfma_f32_16x16x32_bf16 v[96:99], v[146:149], v[154:157], v[96:99]
	v_mfma_f32_16x16x32_bf16 v[120:123], v[136:139], v[170:173], v[120:123]
	v_mfma_f32_16x16x32_bf16 v[88:91], v[146:149], v[170:173], v[88:91]
	v_mfma_f32_16x16x32_bf16 v[112:115], v[136:139], v[194:197], v[112:115]
	v_mfma_f32_16x16x32_bf16 v[80:83], v[146:149], v[194:197], v[80:83]
	v_mfma_f32_16x16x32_bf16 v[104:107], v[136:139], v[202:205], v[104:107]
	v_mfma_f32_16x16x32_bf16 v[72:75], v[146:149], v[202:205], v[72:75]
	s_barrier
	s_add_i32 s14, 0, 0x1c000
	s_add_u32 s66, s66, 0x80
	v_add_u32_e32 v0, s14, v163
	s_addc_u32 s67, s67, 0
	ds_read_b128 v[206:209], v0
	ds_read_b128 v[210:213], v0 offset:1024
	ds_read_b128 v[214:217], v0 offset:2048
	ds_read_b128 v[218:221], v0 offset:3072
	s_mov_b64 s[86:87], s[66:67]
	v_mov_b32_e32 v0, v160
	s_add_i32 s15, vcc_lo, s17
	s_mov_b32 m0, s15
	s_nop 0
	global_load_lds_dwordx4 v0, s[86:87]
	v_mov_b32_e32 v0, v161
	s_add_i32 m0, s15, 0x2000
	s_nop 0
	global_load_lds_dwordx4 v0, s[86:87]
	s_barrier
; template <class Epi, class Sched>
; __device__ __forceinline__ void gemm_phase(LAS unsigned char* lds, const int K_, const Sched& S, const Epi& E, const int wave_) {
;     ...
;         int t = 0;
;         if (Epi::NSTORE > 0 && hoisted) { PG8_BODY(true); t = 2; }
;         for (; t < nt; t += 2) { PG8_BODY(false); }
	s_waitcnt lgkmcnt(0)
	s_waitcnt lgkmcnt(0)
	v_mfma_f32_16x16x32_bf16 v[64:67], v[206:209], v[150:153], v[64:67]
	v_mfma_f32_16x16x32_bf16 v[32:35], v[214:217], v[150:153], v[32:35]
	v_mfma_f32_16x16x32_bf16 v[56:59], v[206:209], v[166:169], v[56:59]
	v_mfma_f32_16x16x32_bf16 v[24:27], v[214:217], v[166:169], v[24:27]
	v_mfma_f32_16x16x32_bf16 v[48:51], v[206:209], v[190:193], v[48:51]
	v_mfma_f32_16x16x32_bf16 v[16:19], v[214:217], v[190:193], v[16:19]
	v_mfma_f32_16x16x32_bf16 v[40:43], v[206:209], v[198:201], v[40:43]
	v_mfma_f32_16x16x32_bf16 v[8:11], v[214:217], v[198:201], v[8:11]
	v_mfma_f32_16x16x32_bf16 v[64:67], v[210:213], v[154:157], v[64:67]
	v_mfma_f32_16x16x32_bf16 v[32:35], v[218:221], v[154:157], v[32:35]
	v_mfma_f32_16x16x32_bf16 v[56:59], v[210:213], v[170:173], v[56:59]
	v_mfma_f32_16x16x32_bf16 v[24:27], v[218:221], v[170:173], v[24:27]
	v_mfma_f32_16x16x32_bf16 v[48:51], v[210:213], v[194:197], v[48:51]
	v_mfma_f32_16x16x32_bf16 v[16:19], v[218:221], v[194:197], v[16:19]
	v_mfma_f32_16x16x32_bf16 v[40:43], v[210:213], v[202:205], v[40:43]
	v_mfma_f32_16x16x32_bf16 v[8:11], v[218:221], v[202:205], v[8:11]
	s_add_u32 s84, s84, 0x80
	s_addc_u32 s85, s85, 0
	v_mov_b32_e32 v0, v160
	s_mov_b32 m0, s71
	s_barrier
	ds_read_b128 v[150:153], v165 offset:49152
	ds_read_b128 v[154:157], v165 offset:50176
	ds_read_b128 v[166:169], v165 offset:51200
	ds_read_b128 v[170:173], v165 offset:52224
	ds_read_b128 v[190:193], v165 offset:53248
	ds_read_b128 v[194:197], v165 offset:54272
	ds_read_b128 v[198:201], v165 offset:55296
	ds_read_b128 v[202:205], v165 offset:56320
	s_nop 0
	global_load_lds_dwordx4 v0, s[84:85]
	v_mov_b32_e32 v0, v161
	s_mov_b32 m0, s75
	s_nop 0
	global_load_lds_dwordx4 v0, s[84:85]
	s_barrier
	s_waitcnt lgkmcnt(0)
	s_waitcnt lgkmcnt(0)
	v_mfma_f32_16x16x32_bf16 v[124:127], v[132:135], v[150:153], v[124:127]
	v_mfma_f32_16x16x32_bf16 v[92:95], v[140:143], v[150:153], v[92:95]
	v_mfma_f32_16x16x32_bf16 v[116:119], v[132:135], v[166:169], v[116:119]
	v_mfma_f32_16x16x32_bf16 v[84:87], v[140:143], v[166:169], v[84:87]
	v_mfma_f32_16x16x32_bf16 v[108:111], v[132:135], v[190:193], v[108:111]
	v_mfma_f32_16x16x32_bf16 v[76:79], v[140:143], v[190:193], v[76:79]
	v_mfma_f32_16x16x32_bf16 v[100:103], v[132:135], v[198:201], v[100:103]
	v_mfma_f32_16x16x32_bf16 v[68:71], v[140:143], v[198:201], v[68:71]
	v_mfma_f32_16x16x32_bf16 v[124:127], v[136:139], v[154:157], v[124:127]
	v_mfma_f32_16x16x32_bf16 v[92:95], v[146:149], v[154:157], v[92:95]
	v_mfma_f32_16x16x32_bf16 v[116:119], v[136:139], v[170:173], v[116:119]
	v_mfma_f32_16x16x32_bf16 v[84:87], v[146:149], v[170:173], v[84:87]
	v_mfma_f32_16x16x32_bf16 v[108:111], v[136:139], v[194:197], v[108:111]
	v_mfma_f32_16x16x32_bf16 v[76:79], v[146:149], v[194:197], v[76:79]
	v_mfma_f32_16x16x32_bf16 v[100:103], v[136:139], v[202:205], v[100:103]
	v_mfma_f32_16x16x32_bf16 v[68:71], v[146:149], v[202:205], v[68:71]
	s_barrier
	s_add_u32 s66, s66, s44
	s_addc_u32 s67, s67, s45
	v_mov_b32_e32 v0, v160
	s_add_i32 s14, s14, s17
	s_mov_b32 m0, s14
	s_nop 0
	global_load_lds_dwordx4 v0, s[66:67]
	v_mov_b32_e32 v0, v161
	s_add_i32 m0, s14, 0x2000
	s_nop 0
	global_load_lds_dwordx4 v0, s[66:67]
	s_waitcnt vmcnt(6)
	s_barrier
	v_mfma_f32_16x16x32_bf16 v[60:63], v[206:209], v[150:153], v[60:63]
	v_mfma_f32_16x16x32_bf16 v[28:31], v[214:217], v[150:153], v[28:31]
	v_mfma_f32_16x16x32_bf16 v[52:55], v[206:209], v[166:169], v[52:55]
	v_mfma_f32_16x16x32_bf16 v[20:23], v[214:217], v[166:169], v[20:23]
	v_mfma_f32_16x16x32_bf16 v[44:47], v[206:209], v[190:193], v[44:47]
	v_mfma_f32_16x16x32_bf16 v[12:15], v[214:217], v[190:193], v[12:15]
	v_mfma_f32_16x16x32_bf16 v[36:39], v[206:209], v[198:201], v[36:39]
	v_mfma_f32_16x16x32_bf16 v[4:7], v[214:217], v[198:201], v[4:7]
	v_mfma_f32_16x16x32_bf16 v[60:63], v[210:213], v[154:157], v[60:63]
	v_mfma_f32_16x16x32_bf16 v[28:31], v[218:221], v[154:157], v[28:31]
	v_mfma_f32_16x16x32_bf16 v[52:55], v[210:213], v[170:173], v[52:55]
	v_mfma_f32_16x16x32_bf16 v[20:23], v[218:221], v[170:173], v[20:23]
	v_mfma_f32_16x16x32_bf16 v[44:47], v[210:213], v[194:197], v[44:47]
	v_mfma_f32_16x16x32_bf16 v[12:15], v[218:221], v[194:197], v[12:15]
	v_mfma_f32_16x16x32_bf16 v[36:39], v[210:213], v[202:205], v[36:39]
	v_mfma_f32_16x16x32_bf16 v[4:7], v[218:221], v[202:205], v[4:7]
	s_add_u32 s24, s24, 0x100
	s_addc_u32 s25, s25, 0
	s_cmp_lt_i32 s51, s70
	s_mov_b32 s64, s51
	s_barrier
	s_cbranch_scc1 .LBB0_1242
	s_mov_b32 s89, s18
	s_mov_b32 s19, s68
	s_mov_b32 s68, s22
	s_mov_b32 s18, s23
	s_mov_b32 s23, s38
	v_readlane_b32 s38, v254, 62

; template <class Epi, class Sched>
; __device__ __forceinline__ void gemm_phase(LAS unsigned char* lds, const int K_, const Sched& S, const Epi& E, const int wave_) {
;     ...
;         if (Epi::NSTORE > 0 && hoisted) { PG8_BODY(true); t = 2; }
.LBB0_1538:
	s_add_u32 s10, s4, 0x100
	s_addc_u32 s14, s5, 0
	s_and_b64 s[20:21], s[40:41], exec
	s_cselect_b32 s25, s45, s14
	s_cselect_b32 s24, s44, s10
	s_add_i32 s10, 0, 0x10000
	v_add_u32_e32 v0, s10, v150
	s_waitcnt lgkmcnt(0)
	ds_read_b128 v[132:135], v0
	ds_read_b128 v[158:161], v0 offset:1024
	ds_read_b128 v[162:165], v0 offset:2048
	ds_read_b128 v[166:169], v0 offset:3072
	ds_read_b128 v[170:173], v152
	ds_read_b128 v[190:193], v152 offset:1024
	ds_read_b128 v[194:197], v152 offset:2048
	ds_read_b128 v[198:201], v152 offset:3072
	ds_read_b128 v[202:205], v152 offset:4096
	ds_read_b128 v[206:209], v152 offset:5120
	ds_read_b128 v[210:213], v152 offset:6144
	ds_read_b128 v[214:217], v152 offset:7168
	s_waitcnt lgkmcnt(8)
	s_barrier
	s_waitcnt lgkmcnt(0)
	s_waitcnt lgkmcnt(0)
	v_mfma_f32_16x16x32_bf16 v[4:7], v[132:135], v[170:173], v[4:7]
	v_mfma_f32_16x16x32_bf16 v[8:11], v[162:165], v[170:173], v[8:11]
	v_mfma_f32_16x16x32_bf16 v[12:15], v[132:135], v[194:197], v[12:15]
	v_mfma_f32_16x16x32_bf16 v[16:19], v[162:165], v[194:197], v[16:19]
	v_mfma_f32_16x16x32_bf16 v[20:23], v[132:135], v[202:205], v[20:23]
	v_mfma_f32_16x16x32_bf16 v[24:27], v[162:165], v[202:205], v[24:27]
	v_mfma_f32_16x16x32_bf16 v[28:31], v[132:135], v[210:213], v[28:31]
	v_mfma_f32_16x16x32_bf16 v[32:35], v[162:165], v[210:213], v[32:35]
	v_mfma_f32_16x16x32_bf16 v[4:7], v[158:161], v[190:193], v[4:7]
	v_mfma_f32_16x16x32_bf16 v[8:11], v[166:169], v[190:193], v[8:11]
	v_mfma_f32_16x16x32_bf16 v[12:15], v[158:161], v[198:201], v[12:15]
	v_mfma_f32_16x16x32_bf16 v[16:19], v[166:169], v[198:201], v[16:19]
	v_mfma_f32_16x16x32_bf16 v[20:23], v[158:161], v[206:209], v[20:23]
	v_mfma_f32_16x16x32_bf16 v[24:27], v[166:169], v[206:209], v[24:27]
	v_mfma_f32_16x16x32_bf16 v[28:31], v[158:161], v[214:217], v[28:31]
	v_mfma_f32_16x16x32_bf16 v[32:35], v[166:169], v[214:217], v[32:35]
	s_barrier
	s_add_i32 s14, 0, 0x14000
	v_add_u32_e32 v0, s14, v150
	ds_read_b128 v[218:221], v0
	ds_read_b128 v[222:225], v0 offset:1024
	ds_read_b128 v[226:229], v0 offset:2048
	ds_read_b128 v[230:233], v0 offset:3072
	s_mov_b64 s[20:21], s[24:25]
	v_mov_b32_e32 v0, v142
	s_add_i32 s10, s10, s26
	s_mov_b32 m0, s10
	s_nop 0
	global_load_lds_dwordx4 v0, s[20:21]
	v_mov_b32_e32 v0, v143
	s_add_i32 m0, s10, 0x2000
	s_nop 0
	global_load_lds_dwordx4 v0, s[20:21]
	s_barrier
	s_waitcnt lgkmcnt(0)
	s_waitcnt lgkmcnt(0)
	v_mfma_f32_16x16x32_bf16 v[40:43], v[218:221], v[170:173], v[40:43]
	v_mfma_f32_16x16x32_bf16 v[44:47], v[226:229], v[170:173], v[44:47]
	v_mfma_f32_16x16x32_bf16 v[48:51], v[218:221], v[194:197], v[48:51]
	v_mfma_f32_16x16x32_bf16 v[52:55], v[226:229], v[194:197], v[52:55]
	v_mfma_f32_16x16x32_bf16 v[56:59], v[218:221], v[202:205], v[56:59]
	v_mfma_f32_16x16x32_bf16 v[60:63], v[226:229], v[202:205], v[60:63]
	v_mfma_f32_16x16x32_bf16 v[68:71], v[218:221], v[210:213], v[68:71]
	v_mfma_f32_16x16x32_bf16 v[76:79], v[226:229], v[210:213], v[76:79]
	v_mfma_f32_16x16x32_bf16 v[40:43], v[222:225], v[190:193], v[40:43]
	v_mfma_f32_16x16x32_bf16 v[44:47], v[230:233], v[190:193], v[44:47]
	v_mfma_f32_16x16x32_bf16 v[48:51], v[222:225], v[198:201], v[48:51]
	v_mfma_f32_16x16x32_bf16 v[52:55], v[230:233], v[198:201], v[52:55]
	v_mfma_f32_16x16x32_bf16 v[56:59], v[222:225], v[206:209], v[56:59]
	v_mfma_f32_16x16x32_bf16 v[60:63], v[230:233], v[206:209], v[60:63]
	v_mfma_f32_16x16x32_bf16 v[68:71], v[222:225], v[214:217], v[68:71]
	v_mfma_f32_16x16x32_bf16 v[76:79], v[230:233], v[214:217], v[76:79]
	v_cndmask_b32_e64 v0, v147, v153, s[40:41]
	s_mov_b64 s[20:21], s[6:7]
	v_mov_b32_e32 v157, v0
	s_mov_b32 m0, s27
	s_barrier
	ds_read_b128 v[170:173], v152 offset:16384
	ds_read_b128 v[190:193], v152 offset:17408
	ds_read_b128 v[194:197], v152 offset:18432
	ds_read_b128 v[198:201], v152 offset:19456
	ds_read_b128 v[202:205], v152 offset:20480
	ds_read_b128 v[206:209], v152 offset:21504
	ds_read_b128 v[210:213], v152 offset:22528
	ds_read_b128 v[214:217], v152 offset:23552
	v_cndmask_b32_e64 v1, v145, v154, s[40:41]
	s_nop 0
	global_load_lds_dwordx4 v157, s[20:21]
	v_mov_b32_e32 v157, v1
	s_mov_b32 m0, s52
	s_nop 0
	global_load_lds_dwordx4 v157, s[20:21]
	s_barrier
	s_waitcnt lgkmcnt(0)
	s_waitcnt lgkmcnt(0)
	v_mfma_f32_16x16x32_bf16 v[64:67], v[132:135], v[170:173], v[64:67]
	v_mfma_f32_16x16x32_bf16 v[72:75], v[162:165], v[170:173], v[72:75]
	v_mfma_f32_16x16x32_bf16 v[80:83], v[132:135], v[194:197], v[80:83]
	v_mfma_f32_16x16x32_bf16 v[84:87], v[162:165], v[194:197], v[84:87]
	v_mfma_f32_16x16x32_bf16 v[88:91], v[132:135], v[202:205], v[88:91]
	v_mfma_f32_16x16x32_bf16 v[92:95], v[162:165], v[202:205], v[92:95]
	v_mfma_f32_16x16x32_bf16 v[96:99], v[132:135], v[210:213], v[96:99]
	v_mfma_f32_16x16x32_bf16 v[100:103], v[162:165], v[210:213], v[100:103]
	v_mfma_f32_16x16x32_bf16 v[64:67], v[158:161], v[190:193], v[64:67]
	v_mfma_f32_16x16x32_bf16 v[72:75], v[166:169], v[190:193], v[72:75]
	v_mfma_f32_16x16x32_bf16 v[80:83], v[158:161], v[198:201], v[80:83]
	v_mfma_f32_16x16x32_bf16 v[84:87], v[166:169], v[198:201], v[84:87]
	v_mfma_f32_16x16x32_bf16 v[88:91], v[158:161], v[206:209], v[88:91]
	v_mfma_f32_16x16x32_bf16 v[92:95], v[166:169], v[206:209], v[92:95]
	v_mfma_f32_16x16x32_bf16 v[96:99], v[158:161], v[214:217], v[96:99]
	v_mfma_f32_16x16x32_bf16 v[100:103], v[166:169], v[214:217], v[100:103]
	s_barrier
	s_add_u32 s20, s24, s0
	s_addc_u32 s21, s25, s1
	v_mov_b32_e32 v132, v142
	s_add_i32 s10, s14, s26
	s_mov_b32 m0, s10
	s_nop 0
	global_load_lds_dwordx4 v132, s[20:21]
	v_mov_b32_e32 v132, v143
	s_add_i32 m0, s10, 0x2000
	s_nop 0
	global_load_lds_dwordx4 v132, s[20:21]
	s_waitcnt vmcnt(14)
	s_barrier
	v_mfma_f32_16x16x32_bf16 v[104:107], v[218:221], v[170:173], v[104:107]
	v_mfma_f32_16x16x32_bf16 v[108:111], v[226:229], v[170:173], v[108:111]
	v_mfma_f32_16x16x32_bf16 v[112:115], v[218:221], v[194:197], v[112:115]
	v_mfma_f32_16x16x32_bf16 v[116:119], v[226:229], v[194:197], v[116:119]
	v_mfma_f32_16x16x32_bf16 v[120:123], v[218:221], v[202:205], v[120:123]
	v_mfma_f32_16x16x32_bf16 v[124:127], v[226:229], v[202:205], v[124:127]
	v_mfma_f32_16x16x32_bf16 v[128:131], v[218:221], v[210:213], v[128:131]
	v_mfma_f32_16x16x32_bf16 v[36:39], v[226:229], v[210:213], v[36:39]
	v_mfma_f32_16x16x32_bf16 v[104:107], v[222:225], v[190:193], v[104:107]
	v_mfma_f32_16x16x32_bf16 v[108:111], v[230:233], v[190:193], v[108:111]
	v_mfma_f32_16x16x32_bf16 v[112:115], v[222:225], v[198:201], v[112:115]
	v_mfma_f32_16x16x32_bf16 v[116:119], v[230:233], v[198:201], v[116:119]
	v_mfma_f32_16x16x32_bf16 v[120:123], v[222:225], v[206:209], v[120:123]
	v_mfma_f32_16x16x32_bf16 v[124:127], v[230:233], v[206:209], v[124:127]
	v_mfma_f32_16x16x32_bf16 v[128:131], v[222:225], v[214:217], v[128:131]
	v_mfma_f32_16x16x32_bf16 v[36:39], v[230:233], v[214:217], v[36:39]
	s_add_i32 s10, 0, 0x18000
	v_add_u32_e32 v157, s10, v150
	s_barrier
	ds_read_b128 v[132:135], v157
	ds_read_b128 v[158:161], v157 offset:1024
	ds_read_b128 v[162:165], v157 offset:2048
	ds_read_b128 v[166:169], v157 offset:3072
	s_mov_b32 m0, s53
	v_cndmask_b32_e64 v157, v146, v155, s[40:41]
	s_mov_b64 s[20:21], s[6:7]
	ds_read_b128 v[170:173], v152 offset:32768
	ds_read_b128 v[190:193], v152 offset:33792
	ds_read_b128 v[194:197], v152 offset:34816
	ds_read_b128 v[198:201], v152 offset:35840
	ds_read_b128 v[202:205], v152 offset:36864
	ds_read_b128 v[206:209], v152 offset:37888
	ds_read_b128 v[210:213], v152 offset:38912
	ds_read_b128 v[214:217], v152 offset:39936
	v_cndmask_b32_e64 v182, v148, v156, s[40:41]
	s_nop 0
	global_load_lds_dwordx4 v157, s[20:21]
	s_mov_b32 m0, s54
	s_nop 0
	global_load_lds_dwordx4 v182, s[20:21]
	s_waitcnt lgkmcnt(8)
	s_barrier
	s_waitcnt lgkmcnt(0)
	s_waitcnt lgkmcnt(0)
	v_mfma_f32_16x16x32_bf16 v[4:7], v[132:135], v[170:173], v[4:7]
	v_mfma_f32_16x16x32_bf16 v[8:11], v[162:165], v[170:173], v[8:11]
	v_mfma_f32_16x16x32_bf16 v[12:15], v[132:135], v[194:197], v[12:15]
	v_mfma_f32_16x16x32_bf16 v[16:19], v[162:165], v[194:197], v[16:19]
	v_mfma_f32_16x16x32_bf16 v[20:23], v[132:135], v[202:205], v[20:23]
	v_mfma_f32_16x16x32_bf16 v[24:27], v[162:165], v[202:205], v[24:27]
	v_mfma_f32_16x16x32_bf16 v[28:31], v[132:135], v[210:213], v[28:31]
	v_mfma_f32_16x16x32_bf16 v[32:35], v[162:165], v[210:213], v[32:35]
	v_mfma_f32_16x16x32_bf16 v[4:7], v[158:161], v[190:193], v[4:7]
	v_mfma_f32_16x16x32_bf16 v[8:11], v[166:169], v[190:193], v[8:11]
	v_mfma_f32_16x16x32_bf16 v[12:15], v[158:161], v[198:201], v[12:15]
	v_mfma_f32_16x16x32_bf16 v[16:19], v[166:169], v[198:201], v[16:19]
	v_mfma_f32_16x16x32_bf16 v[20:23], v[158:161], v[206:209], v[20:23]
	v_mfma_f32_16x16x32_bf16 v[24:27], v[166:169], v[206:209], v[24:27]
	v_mfma_f32_16x16x32_bf16 v[28:31], v[158:161], v[214:217], v[28:31]
	v_mfma_f32_16x16x32_bf16 v[32:35], v[166:169], v[214:217], v[32:35]
	s_barrier
	s_add_i32 s14, 0, 0x1c000
	s_add_u32 s20, s24, 0x80
	v_add_u32_e32 v157, s14, v150
	s_addc_u32 s21, s25, 0
	ds_read_b128 v[218:221], v157
	ds_read_b128 v[222:225], v157 offset:1024
	ds_read_b128 v[226:229], v157 offset:2048
	ds_read_b128 v[230:233], v157 offset:3072
	s_mov_b64 s[24:25], s[20:21]
	v_mov_b32_e32 v157, v142
	s_add_i32 s10, s10, s26
	s_mov_b32 m0, s10
	s_nop 0
	global_load_lds_dwordx4 v157, s[24:25]
	v_mov_b32_e32 v157, v143
	s_add_i32 m0, s10, 0x2000
	s_nop 0
	global_load_lds_dwordx4 v157, s[24:25]
	s_barrier
; template <class Epi, class Sched>
; __device__ __forceinline__ void gemm_phase(LAS unsigned char* lds, const int K_, const Sched& S, const Epi& E, const int wave_) {
;     ...
;         int t = 0;
;         if (Epi::NSTORE > 0 && hoisted) { PG8_BODY(true); t = 2; }
;         for (; t < nt; t += 2) { PG8_BODY(false); }
	s_waitcnt lgkmcnt(0)
	s_waitcnt lgkmcnt(0)
	v_mfma_f32_16x16x32_bf16 v[40:43], v[218:221], v[170:173], v[40:43]
	v_mfma_f32_16x16x32_bf16 v[44:47], v[226:229], v[170:173], v[44:47]
	v_mfma_f32_16x16x32_bf16 v[48:51], v[218:221], v[194:197], v[48:51]
	v_mfma_f32_16x16x32_bf16 v[52:55], v[226:229], v[194:197], v[52:55]
	v_mfma_f32_16x16x32_bf16 v[56:59], v[218:221], v[202:205], v[56:59]
	v_mfma_f32_16x16x32_bf16 v[60:63], v[226:229], v[202:205], v[60:63]
	v_mfma_f32_16x16x32_bf16 v[68:71], v[218:221], v[210:213], v[68:71]
	v_mfma_f32_16x16x32_bf16 v[76:79], v[226:229], v[210:213], v[76:79]
	v_mfma_f32_16x16x32_bf16 v[40:43], v[222:225], v[190:193], v[40:43]
	v_mfma_f32_16x16x32_bf16 v[44:47], v[230:233], v[190:193], v[44:47]
	v_mfma_f32_16x16x32_bf16 v[48:51], v[222:225], v[198:201], v[48:51]
	v_mfma_f32_16x16x32_bf16 v[52:55], v[230:233], v[198:201], v[52:55]
	v_mfma_f32_16x16x32_bf16 v[56:59], v[222:225], v[206:209], v[56:59]
	v_mfma_f32_16x16x32_bf16 v[60:63], v[230:233], v[206:209], v[60:63]
	v_mfma_f32_16x16x32_bf16 v[68:71], v[222:225], v[214:217], v[68:71]
	v_mfma_f32_16x16x32_bf16 v[76:79], v[230:233], v[214:217], v[76:79]
	s_mov_b64 s[24:25], s[8:9]
	s_mov_b32 m0, s56
	s_barrier
	ds_read_b128 v[170:173], v152 offset:49152
	ds_read_b128 v[190:193], v152 offset:50176
	ds_read_b128 v[194:197], v152 offset:51200
	ds_read_b128 v[198:201], v152 offset:52224
	ds_read_b128 v[202:205], v152 offset:53248
	ds_read_b128 v[206:209], v152 offset:54272
	ds_read_b128 v[210:213], v152 offset:55296
	ds_read_b128 v[214:217], v152 offset:56320
	s_nop 0
	global_load_lds_dwordx4 v0, s[24:25]
	s_mov_b32 m0, s57
	s_nop 0
	global_load_lds_dwordx4 v1, s[24:25]
	s_barrier
	s_waitcnt lgkmcnt(0)
	s_waitcnt lgkmcnt(0)
	v_mfma_f32_16x16x32_bf16 v[64:67], v[132:135], v[170:173], v[64:67]
	v_mfma_f32_16x16x32_bf16 v[72:75], v[162:165], v[170:173], v[72:75]
	v_mfma_f32_16x16x32_bf16 v[80:83], v[132:135], v[194:197], v[80:83]
	v_mfma_f32_16x16x32_bf16 v[84:87], v[162:165], v[194:197], v[84:87]
	v_mfma_f32_16x16x32_bf16 v[88:91], v[132:135], v[202:205], v[88:91]
	v_mfma_f32_16x16x32_bf16 v[92:95], v[162:165], v[202:205], v[92:95]
	v_mfma_f32_16x16x32_bf16 v[96:99], v[132:135], v[210:213], v[96:99]
	v_mfma_f32_16x16x32_bf16 v[100:103], v[162:165], v[210:213], v[100:103]
	v_mfma_f32_16x16x32_bf16 v[64:67], v[158:161], v[190:193], v[64:67]
	v_mfma_f32_16x16x32_bf16 v[72:75], v[166:169], v[190:193], v[72:75]
	v_mfma_f32_16x16x32_bf16 v[80:83], v[158:161], v[198:201], v[80:83]
	v_mfma_f32_16x16x32_bf16 v[84:87], v[166:169], v[198:201], v[84:87]
	v_mfma_f32_16x16x32_bf16 v[88:91], v[158:161], v[206:209], v[88:91]
	v_mfma_f32_16x16x32_bf16 v[92:95], v[166:169], v[206:209], v[92:95]
	v_mfma_f32_16x16x32_bf16 v[96:99], v[158:161], v[214:217], v[96:99]
	v_mfma_f32_16x16x32_bf16 v[100:103], v[166:169], v[214:217], v[100:103]
	s_barrier
	s_add_u32 s20, s20, s0
	s_addc_u32 s21, s21, s1
	v_mov_b32_e32 v0, v142
	s_add_i32 s10, s14, s26
	s_mov_b32 m0, s10
	s_nop 0
	global_load_lds_dwordx4 v0, s[20:21]
	v_mov_b32_e32 v0, v143
	s_add_i32 m0, s10, 0x2000
	s_nop 0
	global_load_lds_dwordx4 v0, s[20:21]
	s_waitcnt vmcnt(6)
	s_barrier
	v_mfma_f32_16x16x32_bf16 v[104:107], v[218:221], v[170:173], v[104:107]
	v_mfma_f32_16x16x32_bf16 v[108:111], v[226:229], v[170:173], v[108:111]
	v_mfma_f32_16x16x32_bf16 v[112:115], v[218:221], v[194:197], v[112:115]
	v_mfma_f32_16x16x32_bf16 v[116:119], v[226:229], v[194:197], v[116:119]
	v_mfma_f32_16x16x32_bf16 v[120:123], v[218:221], v[202:205], v[120:123]
	v_mfma_f32_16x16x32_bf16 v[124:127], v[226:229], v[202:205], v[124:127]
	v_mfma_f32_16x16x32_bf16 v[128:131], v[218:221], v[210:213], v[128:131]
	v_mfma_f32_16x16x32_bf16 v[36:39], v[226:229], v[210:213], v[36:39]
	v_mfma_f32_16x16x32_bf16 v[104:107], v[222:225], v[190:193], v[104:107]
	v_mfma_f32_16x16x32_bf16 v[108:111], v[230:233], v[190:193], v[108:111]
	v_mfma_f32_16x16x32_bf16 v[112:115], v[222:225], v[198:201], v[112:115]
	v_mfma_f32_16x16x32_bf16 v[116:119], v[230:233], v[198:201], v[116:119]
	v_mfma_f32_16x16x32_bf16 v[120:123], v[222:225], v[206:209], v[120:123]
	v_mfma_f32_16x16x32_bf16 v[124:127], v[230:233], v[206:209], v[124:127]
	v_mfma_f32_16x16x32_bf16 v[128:131], v[222:225], v[214:217], v[128:131]
	v_mfma_f32_16x16x32_bf16 v[36:39], v[230:233], v[214:217], v[36:39]
	s_mov_b32 s10, 2
	s_barrier
	s_cmp_ge_i32 s10, s55
	s_cbranch_scc1 .LBB0_1557
	s_branch .LBB0_1555

.LBB0_1556:
	s_cmp_eq_u32 s58, s10
	s_cselect_b64 vcc, -1, 0
	s_add_i32 s10, s10, 2
	s_add_u32 s14, s4, s20
	s_addc_u32 s15, s5, s21
	s_and_b64 s[24:25], vcc, exec
	s_cselect_b32 s25, s45, s15
	s_cselect_b32 s24, s44, s14
	s_add_i32 s14, 0, 0x10000
	v_add_u32_e32 v0, s14, v150
	s_waitcnt lgkmcnt(0)
	ds_read_b128 v[132:135], v0
	ds_read_b128 v[158:161], v0 offset:1024
	ds_read_b128 v[162:165], v0 offset:2048
	ds_read_b128 v[166:169], v0 offset:3072
	s_and_b64 s[30:31], vcc, exec
	s_cselect_b32 s15, 0, s21
	s_cselect_b32 s29, 0, s20
	s_add_u32 s30, s76, s20
	s_addc_u32 s31, s77, s21
	s_add_u32 s30, s30, 0xffffff80
	s_addc_u32 s31, s31, -1
	v_mov_b32_e32 v0, v146
	ds_read_b128 v[170:173], v152
	ds_read_b128 v[190:193], v152 offset:1024
	ds_read_b128 v[194:197], v152 offset:2048
	ds_read_b128 v[198:201], v152 offset:3072
	ds_read_b128 v[202:205], v152 offset:4096
	ds_read_b128 v[206:209], v152 offset:5120
	ds_read_b128 v[210:213], v152 offset:6144
	ds_read_b128 v[214:217], v152 offset:7168
	s_add_i32 m0, s27, 0xc000
	s_nop 0
	global_load_lds_dwordx4 v0, s[30:31]
	v_mov_b32_e32 v0, v148
	s_add_i32 m0, s27, 0xe000
	s_nop 0
	global_load_lds_dwordx4 v0, s[30:31]
	s_waitcnt lgkmcnt(8)
	s_barrier
	s_waitcnt lgkmcnt(0)
	s_waitcnt lgkmcnt(0)
	v_mfma_f32_16x16x32_bf16 v[4:7], v[132:135], v[170:173], v[4:7]
	v_mfma_f32_16x16x32_bf16 v[8:11], v[162:165], v[170:173], v[8:11]
	v_mfma_f32_16x16x32_bf16 v[12:15], v[132:135], v[194:197], v[12:15]
	v_mfma_f32_16x16x32_bf16 v[16:19], v[162:165], v[194:197], v[16:19]
	v_mfma_f32_16x16x32_bf16 v[20:23], v[132:135], v[202:205], v[20:23]
	v_mfma_f32_16x16x32_bf16 v[24:27], v[162:165], v[202:205], v[24:27]
	v_mfma_f32_16x16x32_bf16 v[28:31], v[132:135], v[210:213], v[28:31]
	v_mfma_f32_16x16x32_bf16 v[32:35], v[162:165], v[210:213], v[32:35]
	v_mfma_f32_16x16x32_bf16 v[4:7], v[158:161], v[190:193], v[4:7]
	v_mfma_f32_16x16x32_bf16 v[8:11], v[166:169], v[190:193], v[8:11]
	v_mfma_f32_16x16x32_bf16 v[12:15], v[158:161], v[198:201], v[12:15]
	v_mfma_f32_16x16x32_bf16 v[16:19], v[166:169], v[198:201], v[16:19]
	v_mfma_f32_16x16x32_bf16 v[20:23], v[158:161], v[206:209], v[20:23]
	v_mfma_f32_16x16x32_bf16 v[24:27], v[166:169], v[206:209], v[24:27]
	v_mfma_f32_16x16x32_bf16 v[28:31], v[158:161], v[214:217], v[28:31]
	v_mfma_f32_16x16x32_bf16 v[32:35], v[166:169], v[214:217], v[32:35]
	s_barrier
	s_add_i32 s47, 0, 0x14000
	v_add_u32_e32 v0, s47, v150
	ds_read_b128 v[218:221], v0
	ds_read_b128 v[222:225], v0 offset:1024
	ds_read_b128 v[226:229], v0 offset:2048
	ds_read_b128 v[230:233], v0 offset:3072
	s_mov_b64 s[30:31], s[24:25]
	v_mov_b32_e32 v0, v142
	s_add_i32 s14, s14, s26
	s_mov_b32 m0, s14
	s_nop 0
	global_load_lds_dwordx4 v0, s[30:31]
	v_mov_b32_e32 v0, v143
	s_add_i32 m0, s14, 0x2000
	s_nop 0
	global_load_lds_dwordx4 v0, s[30:31]
	s_barrier
	s_waitcnt lgkmcnt(0)
	s_waitcnt lgkmcnt(0)
	v_mfma_f32_16x16x32_bf16 v[40:43], v[218:221], v[170:173], v[40:43]
	v_mfma_f32_16x16x32_bf16 v[44:47], v[226:229], v[170:173], v[44:47]
	v_mfma_f32_16x16x32_bf16 v[48:51], v[218:221], v[194:197], v[48:51]
	v_mfma_f32_16x16x32_bf16 v[52:55], v[226:229], v[194:197], v[52:55]
	v_mfma_f32_16x16x32_bf16 v[56:59], v[218:221], v[202:205], v[56:59]
	v_mfma_f32_16x16x32_bf16 v[60:63], v[226:229], v[202:205], v[60:63]
	v_mfma_f32_16x16x32_bf16 v[68:71], v[218:221], v[210:213], v[68:71]
	v_mfma_f32_16x16x32_bf16 v[76:79], v[226:229], v[210:213], v[76:79]
	v_mfma_f32_16x16x32_bf16 v[40:43], v[222:225], v[190:193], v[40:43]
	v_mfma_f32_16x16x32_bf16 v[44:47], v[230:233], v[190:193], v[44:47]
	v_mfma_f32_16x16x32_bf16 v[48:51], v[222:225], v[198:201], v[48:51]
	v_mfma_f32_16x16x32_bf16 v[52:55], v[230:233], v[198:201], v[52:55]
	v_mfma_f32_16x16x32_bf16 v[56:59], v[222:225], v[206:209], v[56:59]
	v_mfma_f32_16x16x32_bf16 v[60:63], v[230:233], v[206:209], v[60:63]
	v_mfma_f32_16x16x32_bf16 v[68:71], v[222:225], v[214:217], v[68:71]
	v_mfma_f32_16x16x32_bf16 v[76:79], v[230:233], v[214:217], v[76:79]
	s_add_u32 s50, s76, s29
	v_cndmask_b32_e32 v0, v147, v153, vcc
	s_addc_u32 s51, s77, s15
	s_mov_b64 s[30:31], s[50:51]
	v_mov_b32_e32 v157, v0
	s_mov_b32 m0, s27
	s_barrier
	ds_read_b128 v[170:173], v152 offset:16384
	ds_read_b128 v[190:193], v152 offset:17408
	ds_read_b128 v[194:197], v152 offset:18432
	ds_read_b128 v[198:201], v152 offset:19456
	ds_read_b128 v[202:205], v152 offset:20480
	ds_read_b128 v[206:209], v152 offset:21504
	ds_read_b128 v[210:213], v152 offset:22528
	ds_read_b128 v[214:217], v152 offset:23552
	v_cndmask_b32_e32 v1, v145, v154, vcc
	s_nop 0
	global_load_lds_dwordx4 v157, s[30:31]
	v_mov_b32_e32 v157, v1
	s_mov_b32 m0, s52
	s_nop 0
	global_load_lds_dwordx4 v157, s[30:31]
	s_barrier
	s_waitcnt lgkmcnt(0)
	s_waitcnt lgkmcnt(0)
	v_mfma_f32_16x16x32_bf16 v[64:67], v[132:135], v[170:173], v[64:67]
	v_mfma_f32_16x16x32_bf16 v[72:75], v[162:165], v[170:173], v[72:75]
	v_mfma_f32_16x16x32_bf16 v[80:83], v[132:135], v[194:197], v[80:83]
	v_mfma_f32_16x16x32_bf16 v[84:87], v[162:165], v[194:197], v[84:87]
	v_mfma_f32_16x16x32_bf16 v[88:91], v[132:135], v[202:205], v[88:91]
	v_mfma_f32_16x16x32_bf16 v[92:95], v[162:165], v[202:205], v[92:95]
	v_mfma_f32_16x16x32_bf16 v[96:99], v[132:135], v[210:213], v[96:99]
	v_mfma_f32_16x16x32_bf16 v[100:103], v[162:165], v[210:213], v[100:103]
	v_mfma_f32_16x16x32_bf16 v[64:67], v[158:161], v[190:193], v[64:67]
	v_mfma_f32_16x16x32_bf16 v[72:75], v[166:169], v[190:193], v[72:75]
	v_mfma_f32_16x16x32_bf16 v[80:83], v[158:161], v[198:201], v[80:83]
	v_mfma_f32_16x16x32_bf16 v[84:87], v[166:169], v[198:201], v[84:87]
	v_mfma_f32_16x16x32_bf16 v[88:91], v[158:161], v[206:209], v[88:91]
	v_mfma_f32_16x16x32_bf16 v[92:95], v[166:169], v[206:209], v[92:95]
	v_mfma_f32_16x16x32_bf16 v[96:99], v[158:161], v[214:217], v[96:99]
	v_mfma_f32_16x16x32_bf16 v[100:103], v[166:169], v[214:217], v[100:103]
	s_barrier
	s_add_u32 s30, s24, s0
	s_addc_u32 s31, s25, s1
	v_mov_b32_e32 v132, v142
	s_add_i32 s14, s47, s26
	s_mov_b32 m0, s14
	s_nop 0
	global_load_lds_dwordx4 v132, s[30:31]
	v_mov_b32_e32 v132, v143
	s_add_i32 m0, s14, 0x2000
	s_nop 0
	global_load_lds_dwordx4 v132, s[30:31]
	s_waitcnt vmcnt(6)
	s_barrier
	v_mfma_f32_16x16x32_bf16 v[104:107], v[218:221], v[170:173], v[104:107]
	v_mfma_f32_16x16x32_bf16 v[108:111], v[226:229], v[170:173], v[108:111]
	v_mfma_f32_16x16x32_bf16 v[112:115], v[218:221], v[194:197], v[112:115]
	v_mfma_f32_16x16x32_bf16 v[116:119], v[226:229], v[194:197], v[116:119]
	v_mfma_f32_16x16x32_bf16 v[120:123], v[218:221], v[202:205], v[120:123]
	v_mfma_f32_16x16x32_bf16 v[124:127], v[226:229], v[202:205], v[124:127]
	v_mfma_f32_16x16x32_bf16 v[128:131], v[218:221], v[210:213], v[128:131]
	v_mfma_f32_16x16x32_bf16 v[36:39], v[226:229], v[210:213], v[36:39]
	v_mfma_f32_16x16x32_bf16 v[104:107], v[222:225], v[190:193], v[104:107]
	v_mfma_f32_16x16x32_bf16 v[108:111], v[230:233], v[190:193], v[108:111]
	v_mfma_f32_16x16x32_bf16 v[112:115], v[222:225], v[198:201], v[112:115]
	v_mfma_f32_16x16x32_bf16 v[116:119], v[230:233], v[198:201], v[116:119]
	v_mfma_f32_16x16x32_bf16 v[120:123], v[222:225], v[206:209], v[120:123]
	v_mfma_f32_16x16x32_bf16 v[124:127], v[230:233], v[206:209], v[124:127]
	v_mfma_f32_16x16x32_bf16 v[128:131], v[222:225], v[214:217], v[128:131]
	v_mfma_f32_16x16x32_bf16 v[36:39], v[230:233], v[214:217], v[36:39]
	s_add_i32 s14, 0, 0x18000
	v_add_u32_e32 v157, s14, v150
	s_barrier
	ds_read_b128 v[132:135], v157
	ds_read_b128 v[158:161], v157 offset:1024
	ds_read_b128 v[162:165], v157 offset:2048
	ds_read_b128 v[166:169], v157 offset:3072
	s_mov_b32 m0, s53
	v_cndmask_b32_e32 v157, v146, v155, vcc
	s_mov_b64 s[30:31], s[50:51]
	ds_read_b128 v[170:173], v152 offset:32768
	ds_read_b128 v[190:193], v152 offset:33792
	ds_read_b128 v[194:197], v152 offset:34816
	ds_read_b128 v[198:201], v152 offset:35840
	ds_read_b128 v[202:205], v152 offset:36864
	ds_read_b128 v[206:209], v152 offset:37888
	ds_read_b128 v[210:213], v152 offset:38912
	ds_read_b128 v[214:217], v152 offset:39936
	v_cndmask_b32_e32 v182, v148, v156, vcc
	s_nop 0
	global_load_lds_dwordx4 v157, s[30:31]
	s_mov_b32 m0, s54
	s_nop 0
	global_load_lds_dwordx4 v182, s[30:31]
	s_waitcnt lgkmcnt(8)
	s_barrier
	s_waitcnt lgkmcnt(0)
	s_waitcnt lgkmcnt(0)
	v_mfma_f32_16x16x32_bf16 v[4:7], v[132:135], v[170:173], v[4:7]
	v_mfma_f32_16x16x32_bf16 v[8:11], v[162:165], v[170:173], v[8:11]
	v_mfma_f32_16x16x32_bf16 v[12:15], v[132:135], v[194:197], v[12:15]
	v_mfma_f32_16x16x32_bf16 v[16:19], v[162:165], v[194:197], v[16:19]
	v_mfma_f32_16x16x32_bf16 v[20:23], v[132:135], v[202:205], v[20:23]
	v_mfma_f32_16x16x32_bf16 v[24:27], v[162:165], v[202:205], v[24:27]
	v_mfma_f32_16x16x32_bf16 v[28:31], v[132:135], v[210:213], v[28:31]
	v_mfma_f32_16x16x32_bf16 v[32:35], v[162:165], v[210:213], v[32:35]
	v_mfma_f32_16x16x32_bf16 v[4:7], v[158:161], v[190:193], v[4:7]
	v_mfma_f32_16x16x32_bf16 v[8:11], v[166:169], v[190:193], v[8:11]
	v_mfma_f32_16x16x32_bf16 v[12:15], v[158:161], v[198:201], v[12:15]
	v_mfma_f32_16x16x32_bf16 v[16:19], v[166:169], v[198:201], v[16:19]
	v_mfma_f32_16x16x32_bf16 v[20:23], v[158:161], v[206:209], v[20:23]
	v_mfma_f32_16x16x32_bf16 v[24:27], v[166:169], v[206:209], v[24:27]
	v_mfma_f32_16x16x32_bf16 v[28:31], v[158:161], v[214:217], v[28:31]
	v_mfma_f32_16x16x32_bf16 v[32:35], v[166:169], v[214:217], v[32:35]
	s_barrier
	s_add_i32 s15, 0, 0x1c000
	s_add_u32 s24, s24, 0x80
	v_add_u32_e32 v157, s15, v150
	s_addc_u32 s25, s25, 0
	ds_read_b128 v[218:221], v157
	ds_read_b128 v[222:225], v157 offset:1024
	ds_read_b128 v[226:229], v157 offset:2048
	ds_read_b128 v[230:233], v157 offset:3072
	s_mov_b64 s[30:31], s[24:25]
	v_mov_b32_e32 v157, v142
	s_add_i32 s14, s14, s26
	s_mov_b32 m0, s14
	s_nop 0
	global_load_lds_dwordx4 v157, s[30:31]
	v_mov_b32_e32 v157, v143
	s_add_i32 m0, s14, 0x2000
	s_nop 0
	global_load_lds_dwordx4 v157, s[30:31]
	s_barrier
; template <class Epi, class Sched>
; __device__ __forceinline__ void gemm_phase(LAS unsigned char* lds, const int K_, const Sched& S, const Epi& E, const int wave_) {
;     ...
;         int t = 0;
;         if (Epi::NSTORE > 0 && hoisted) { PG8_BODY(true); t = 2; }
;         for (; t < nt; t += 2) { PG8_BODY(false); }
	s_waitcnt lgkmcnt(0)
	s_waitcnt lgkmcnt(0)
	v_mfma_f32_16x16x32_bf16 v[40:43], v[218:221], v[170:173], v[40:43]
	v_mfma_f32_16x16x32_bf16 v[44:47], v[226:229], v[170:173], v[44:47]
	v_mfma_f32_16x16x32_bf16 v[48:51], v[218:221], v[194:197], v[48:51]
	v_mfma_f32_16x16x32_bf16 v[52:55], v[226:229], v[194:197], v[52:55]
	v_mfma_f32_16x16x32_bf16 v[56:59], v[218:221], v[202:205], v[56:59]
	v_mfma_f32_16x16x32_bf16 v[60:63], v[226:229], v[202:205], v[60:63]
	v_mfma_f32_16x16x32_bf16 v[68:71], v[218:221], v[210:213], v[68:71]
	v_mfma_f32_16x16x32_bf16 v[76:79], v[226:229], v[210:213], v[76:79]
	v_mfma_f32_16x16x32_bf16 v[40:43], v[222:225], v[190:193], v[40:43]
	v_mfma_f32_16x16x32_bf16 v[44:47], v[230:233], v[190:193], v[44:47]
	v_mfma_f32_16x16x32_bf16 v[48:51], v[222:225], v[198:201], v[48:51]
	v_mfma_f32_16x16x32_bf16 v[52:55], v[230:233], v[198:201], v[52:55]
	v_mfma_f32_16x16x32_bf16 v[56:59], v[222:225], v[206:209], v[56:59]
	v_mfma_f32_16x16x32_bf16 v[60:63], v[230:233], v[206:209], v[60:63]
	v_mfma_f32_16x16x32_bf16 v[68:71], v[222:225], v[214:217], v[68:71]
	v_mfma_f32_16x16x32_bf16 v[76:79], v[230:233], v[214:217], v[76:79]
	s_add_u32 s30, s50, 0x80
	s_addc_u32 s31, s51, 0
	s_mov_b32 m0, s56
	s_barrier
	ds_read_b128 v[170:173], v152 offset:49152
	ds_read_b128 v[190:193], v152 offset:50176
	ds_read_b128 v[194:197], v152 offset:51200
	ds_read_b128 v[198:201], v152 offset:52224
	ds_read_b128 v[202:205], v152 offset:53248
	ds_read_b128 v[206:209], v152 offset:54272
	ds_read_b128 v[210:213], v152 offset:55296
	ds_read_b128 v[214:217], v152 offset:56320
	s_nop 0
	global_load_lds_dwordx4 v0, s[30:31]
	s_mov_b32 m0, s57
	s_nop 0
	global_load_lds_dwordx4 v1, s[30:31]
	s_barrier
	s_waitcnt lgkmcnt(0)
	s_waitcnt lgkmcnt(0)
	v_mfma_f32_16x16x32_bf16 v[64:67], v[132:135], v[170:173], v[64:67]
	v_mfma_f32_16x16x32_bf16 v[72:75], v[162:165], v[170:173], v[72:75]
	v_mfma_f32_16x16x32_bf16 v[80:83], v[132:135], v[194:197], v[80:83]
	v_mfma_f32_16x16x32_bf16 v[84:87], v[162:165], v[194:197], v[84:87]
	v_mfma_f32_16x16x32_bf16 v[88:91], v[132:135], v[202:205], v[88:91]
	v_mfma_f32_16x16x32_bf16 v[92:95], v[162:165], v[202:205], v[92:95]
	v_mfma_f32_16x16x32_bf16 v[96:99], v[132:135], v[210:213], v[96:99]
	v_mfma_f32_16x16x32_bf16 v[100:103], v[162:165], v[210:213], v[100:103]
	v_mfma_f32_16x16x32_bf16 v[64:67], v[158:161], v[190:193], v[64:67]
	v_mfma_f32_16x16x32_bf16 v[72:75], v[166:169], v[190:193], v[72:75]
	v_mfma_f32_16x16x32_bf16 v[80:83], v[158:161], v[198:201], v[80:83]
	v_mfma_f32_16x16x32_bf16 v[84:87], v[166:169], v[198:201], v[84:87]
	v_mfma_f32_16x16x32_bf16 v[88:91], v[158:161], v[206:209], v[88:91]
	v_mfma_f32_16x16x32_bf16 v[92:95], v[166:169], v[206:209], v[92:95]
	v_mfma_f32_16x16x32_bf16 v[96:99], v[158:161], v[214:217], v[96:99]
	v_mfma_f32_16x16x32_bf16 v[100:103], v[166:169], v[214:217], v[100:103]
	s_barrier
	s_add_u32 s24, s24, s0
	s_addc_u32 s25, s25, s1
	v_mov_b32_e32 v0, v142
	s_add_i32 s14, s15, s26
	s_mov_b32 m0, s14
	s_nop 0
	global_load_lds_dwordx4 v0, s[24:25]
	v_mov_b32_e32 v0, v143
	s_add_i32 m0, s14, 0x2000
	s_nop 0
	global_load_lds_dwordx4 v0, s[24:25]
	s_waitcnt vmcnt(6)
	s_barrier
	v_mfma_f32_16x16x32_bf16 v[104:107], v[218:221], v[170:173], v[104:107]
	v_mfma_f32_16x16x32_bf16 v[108:111], v[226:229], v[170:173], v[108:111]
	v_mfma_f32_16x16x32_bf16 v[112:115], v[218:221], v[194:197], v[112:115]
	v_mfma_f32_16x16x32_bf16 v[116:119], v[226:229], v[194:197], v[116:119]
	v_mfma_f32_16x16x32_bf16 v[120:123], v[218:221], v[202:205], v[120:123]
	v_mfma_f32_16x16x32_bf16 v[124:127], v[226:229], v[202:205], v[124:127]
	v_mfma_f32_16x16x32_bf16 v[128:131], v[218:221], v[210:213], v[128:131]
	v_mfma_f32_16x16x32_bf16 v[36:39], v[226:229], v[210:213], v[36:39]
	v_mfma_f32_16x16x32_bf16 v[104:107], v[222:225], v[190:193], v[104:107]
	v_mfma_f32_16x16x32_bf16 v[108:111], v[230:233], v[190:193], v[108:111]
	v_mfma_f32_16x16x32_bf16 v[112:115], v[222:225], v[198:201], v[112:115]
	v_mfma_f32_16x16x32_bf16 v[116:119], v[230:233], v[198:201], v[116:119]
	v_mfma_f32_16x16x32_bf16 v[120:123], v[222:225], v[206:209], v[120:123]
	v_mfma_f32_16x16x32_bf16 v[124:127], v[230:233], v[206:209], v[124:127]
	v_mfma_f32_16x16x32_bf16 v[128:131], v[222:225], v[214:217], v[128:131]
	v_mfma_f32_16x16x32_bf16 v[36:39], v[230:233], v[214:217], v[36:39]
	s_add_u32 s20, s20, 0x100
	s_addc_u32 s21, s21, 0
	s_cmp_lt_i32 s10, s55
	s_barrier
	s_cbranch_scc1 .LBB0_1556

; template <class Epi, class Sched>
; __device__ __forceinline__ void gemm_phase(LAS unsigned char* lds, const int K_, const Sched& S, const Epi& E, const int wave_) {
;     ...
;         int t = 0;
;         if (Epi::NSTORE > 0 && hoisted) { PG8_BODY(true); t = 2; }
;         for (; t < nt; t += 2) { PG8_BODY(false); }
.LBB0_1628:
	s_add_i32 s31, s24, 2
	s_add_u32 s14, s46, s29
	s_addc_u32 s15, s47, s30
	s_add_i32 s25, 0, 0x10000
	v_add_u32_e32 v0, s25, v137
	s_add_u32 s39, s9, s29
	ds_read_b128 v[140:143], v0
	ds_read_b128 v[146:149], v0 offset:1024
	ds_read_b128 v[150:153], v0 offset:2048
	ds_read_b128 v[154:157], v0 offset:3072
	s_addc_u32 s51, s21, s30
	s_add_u32 s50, s39, 0xffffff80
	s_addc_u32 s51, s51, -1
	s_add_i32 s66, s25, s17
	s_add_i32 m0, s26, 0xc000
	s_add_i32 s39, s26, 0xe000
	s_add_i32 s64, 0, 0x14000
	s_add_i32 s67, s66, 0x2000
	s_cmp_eq_u32 s59, s24
	s_cselect_b32 s24, s42, s14
	s_cselect_b32 s25, s43, s15
	s_cselect_b32 s14, 0, s30
	s_cselect_b32 s15, 0, s29
	v_mov_b32_e32 v0, v132
	ds_read_b128 v[158:161], v139
	ds_read_b128 v[162:165], v139 offset:1024
	ds_read_b128 v[166:169], v139 offset:2048
	ds_read_b128 v[170:173], v139 offset:3072
	ds_read_b128 v[190:193], v139 offset:4096
	ds_read_b128 v[194:197], v139 offset:5120
	ds_read_b128 v[198:201], v139 offset:6144
	ds_read_b128 v[202:205], v139 offset:7168
	s_nop 0
	global_load_lds_dwordx4 v0, s[50:51]
	v_mov_b32_e32 v0, v134
	s_mov_b32 m0, s39
	s_nop 0
	global_load_lds_dwordx4 v0, s[50:51]
	s_waitcnt lgkmcnt(8)
	s_barrier
	s_waitcnt lgkmcnt(0)
	s_waitcnt lgkmcnt(0)
	v_mfma_f32_16x16x32_bf16 v[128:131], v[140:143], v[158:161], v[128:131]
	v_mfma_f32_16x16x32_bf16 v[124:127], v[150:153], v[158:161], v[124:127]
	v_mfma_f32_16x16x32_bf16 v[112:115], v[140:143], v[166:169], v[112:115]
	v_mfma_f32_16x16x32_bf16 v[108:111], v[150:153], v[166:169], v[108:111]
	v_mfma_f32_16x16x32_bf16 v[96:99], v[140:143], v[190:193], v[96:99]
	v_mfma_f32_16x16x32_bf16 v[92:95], v[150:153], v[190:193], v[92:95]
	v_mfma_f32_16x16x32_bf16 v[80:83], v[140:143], v[198:201], v[80:83]
	v_mfma_f32_16x16x32_bf16 v[76:79], v[150:153], v[198:201], v[76:79]
	v_mfma_f32_16x16x32_bf16 v[128:131], v[146:149], v[162:165], v[128:131]
	v_mfma_f32_16x16x32_bf16 v[124:127], v[154:157], v[162:165], v[124:127]
	v_mfma_f32_16x16x32_bf16 v[112:115], v[146:149], v[170:173], v[112:115]
	v_mfma_f32_16x16x32_bf16 v[108:111], v[154:157], v[170:173], v[108:111]
	v_mfma_f32_16x16x32_bf16 v[96:99], v[146:149], v[194:197], v[96:99]
	v_mfma_f32_16x16x32_bf16 v[92:95], v[154:157], v[194:197], v[92:95]
	v_mfma_f32_16x16x32_bf16 v[80:83], v[146:149], v[202:205], v[80:83]
	v_mfma_f32_16x16x32_bf16 v[76:79], v[154:157], v[202:205], v[76:79]
	s_barrier
	v_add_u32_e32 v0, s64, v137
	ds_read_b128 v[206:209], v0
	ds_read_b128 v[210:213], v0 offset:1024
	ds_read_b128 v[214:217], v0 offset:2048
	ds_read_b128 v[218:221], v0 offset:3072
	s_mov_b64 s[50:51], s[24:25]
	v_mov_b32_e32 v0, v133
	s_mov_b32 m0, s66
	s_nop 0
	global_load_lds_dwordx4 v0, s[50:51]
	v_mov_b32_e32 v0, v135
	s_mov_b32 m0, s67
	s_nop 0
	global_load_lds_dwordx4 v0, s[50:51]
	s_barrier
	s_waitcnt lgkmcnt(0)
	s_waitcnt lgkmcnt(0)
	v_mfma_f32_16x16x32_bf16 v[120:123], v[206:209], v[158:161], v[120:123]
	v_mfma_f32_16x16x32_bf16 v[116:119], v[214:217], v[158:161], v[116:119]
	v_mfma_f32_16x16x32_bf16 v[104:107], v[206:209], v[166:169], v[104:107]
	v_mfma_f32_16x16x32_bf16 v[100:103], v[214:217], v[166:169], v[100:103]
	v_mfma_f32_16x16x32_bf16 v[88:91], v[206:209], v[190:193], v[88:91]
	v_mfma_f32_16x16x32_bf16 v[84:87], v[214:217], v[190:193], v[84:87]
	v_mfma_f32_16x16x32_bf16 v[72:75], v[206:209], v[198:201], v[72:75]
	v_mfma_f32_16x16x32_bf16 v[68:71], v[214:217], v[198:201], v[68:71]
	v_mfma_f32_16x16x32_bf16 v[120:123], v[210:213], v[162:165], v[120:123]
	v_mfma_f32_16x16x32_bf16 v[116:119], v[218:221], v[162:165], v[116:119]
	v_mfma_f32_16x16x32_bf16 v[104:107], v[210:213], v[170:173], v[104:107]
	v_mfma_f32_16x16x32_bf16 v[100:103], v[218:221], v[170:173], v[100:103]
	v_mfma_f32_16x16x32_bf16 v[88:91], v[210:213], v[194:197], v[88:91]
	v_mfma_f32_16x16x32_bf16 v[84:87], v[218:221], v[194:197], v[84:87]
	v_mfma_f32_16x16x32_bf16 v[72:75], v[210:213], v[202:205], v[72:75]
	v_mfma_f32_16x16x32_bf16 v[68:71], v[218:221], v[202:205], v[68:71]
	s_cselect_b32 s69, s44, s48
	s_cselect_b32 s39, s45, s49
	s_add_u32 s50, s69, s15
	s_addc_u32 s51, s39, s14
	s_mov_b64 s[66:67], s[50:51]
	v_mov_b32_e32 v0, v132
	s_mov_b32 m0, s26
	s_barrier
	ds_read_b128 v[158:161], v139 offset:16384
	ds_read_b128 v[162:165], v139 offset:17408
	ds_read_b128 v[166:169], v139 offset:18432
	ds_read_b128 v[170:173], v139 offset:19456
	ds_read_b128 v[190:193], v139 offset:20480
	ds_read_b128 v[194:197], v139 offset:21504
	ds_read_b128 v[198:201], v139 offset:22528
	ds_read_b128 v[202:205], v139 offset:23552
	s_nop 0
	global_load_lds_dwordx4 v0, s[66:67]
	v_mov_b32_e32 v0, v134
	s_mov_b32 m0, s27
	s_nop 0
	global_load_lds_dwordx4 v0, s[66:67]
	s_barrier
	s_waitcnt lgkmcnt(0)
	s_waitcnt lgkmcnt(0)
	v_mfma_f32_16x16x32_bf16 v[64:67], v[140:143], v[158:161], v[64:67]
	v_mfma_f32_16x16x32_bf16 v[60:63], v[150:153], v[158:161], v[60:63]
	v_mfma_f32_16x16x32_bf16 v[48:51], v[140:143], v[166:169], v[48:51]
	v_mfma_f32_16x16x32_bf16 v[44:47], v[150:153], v[166:169], v[44:47]
	v_mfma_f32_16x16x32_bf16 v[32:35], v[140:143], v[190:193], v[32:35]
	v_mfma_f32_16x16x32_bf16 v[28:31], v[150:153], v[190:193], v[28:31]
	v_mfma_f32_16x16x32_bf16 v[16:19], v[140:143], v[198:201], v[16:19]
	v_mfma_f32_16x16x32_bf16 v[12:15], v[150:153], v[198:201], v[12:15]
	v_mfma_f32_16x16x32_bf16 v[64:67], v[146:149], v[162:165], v[64:67]
	v_mfma_f32_16x16x32_bf16 v[60:63], v[154:157], v[162:165], v[60:63]
	v_mfma_f32_16x16x32_bf16 v[48:51], v[146:149], v[170:173], v[48:51]
	v_mfma_f32_16x16x32_bf16 v[44:47], v[154:157], v[170:173], v[44:47]
	v_mfma_f32_16x16x32_bf16 v[32:35], v[146:149], v[194:197], v[32:35]
	v_mfma_f32_16x16x32_bf16 v[28:31], v[154:157], v[194:197], v[28:31]
	v_mfma_f32_16x16x32_bf16 v[16:19], v[146:149], v[202:205], v[16:19]
	v_mfma_f32_16x16x32_bf16 v[12:15], v[154:157], v[202:205], v[12:15]
	s_barrier
	s_add_u32 s66, s24, s4
	s_addc_u32 s67, s25, s5
	v_mov_b32_e32 v0, v133
	s_add_i32 s64, s64, s17
	s_mov_b32 m0, s64
	s_nop 0
	global_load_lds_dwordx4 v0, s[66:67]
	v_mov_b32_e32 v0, v135
	s_add_i32 m0, s64, 0x2000
	s_nop 0
	global_load_lds_dwordx4 v0, s[66:67]
	s_waitcnt vmcnt(6)
	s_barrier
	v_mfma_f32_16x16x32_bf16 v[56:59], v[206:209], v[158:161], v[56:59]
	v_mfma_f32_16x16x32_bf16 v[52:55], v[214:217], v[158:161], v[52:55]
	v_mfma_f32_16x16x32_bf16 v[40:43], v[206:209], v[166:169], v[40:43]
	v_mfma_f32_16x16x32_bf16 v[36:39], v[214:217], v[166:169], v[36:39]
	v_mfma_f32_16x16x32_bf16 v[24:27], v[206:209], v[190:193], v[24:27]
	v_mfma_f32_16x16x32_bf16 v[20:23], v[214:217], v[190:193], v[20:23]
	v_mfma_f32_16x16x32_bf16 v[8:11], v[206:209], v[198:201], v[8:11]
	v_mfma_f32_16x16x32_bf16 v[4:7], v[214:217], v[198:201], v[4:7]
	v_mfma_f32_16x16x32_bf16 v[56:59], v[210:213], v[162:165], v[56:59]
	v_mfma_f32_16x16x32_bf16 v[52:55], v[218:221], v[162:165], v[52:55]
	v_mfma_f32_16x16x32_bf16 v[40:43], v[210:213], v[170:173], v[40:43]
	v_mfma_f32_16x16x32_bf16 v[36:39], v[218:221], v[170:173], v[36:39]
	v_mfma_f32_16x16x32_bf16 v[24:27], v[210:213], v[194:197], v[24:27]
	v_mfma_f32_16x16x32_bf16 v[20:23], v[218:221], v[194:197], v[20:23]
	v_mfma_f32_16x16x32_bf16 v[8:11], v[210:213], v[202:205], v[8:11]
	v_mfma_f32_16x16x32_bf16 v[4:7], v[218:221], v[202:205], v[4:7]
	s_add_i32 s64, 0, 0x18000
	v_add_u32_e32 v0, s64, v137
	s_barrier
	ds_read_b128 v[140:143], v0
	ds_read_b128 v[146:149], v0 offset:1024
	ds_read_b128 v[150:153], v0 offset:2048
	ds_read_b128 v[154:157], v0 offset:3072
	s_add_u32 s66, s69, s0
	s_addc_u32 s39, s39, s1
	s_add_u32 s66, s66, s15
	s_addc_u32 s67, s39, s14
	v_mov_b32_e32 v0, v132
	s_mov_b32 m0, s52
	ds_read_b128 v[158:161], v139 offset:32768
	ds_read_b128 v[162:165], v139 offset:33792
	ds_read_b128 v[166:169], v139 offset:34816
	ds_read_b128 v[170:173], v139 offset:35840
	ds_read_b128 v[190:193], v139 offset:36864
	ds_read_b128 v[194:197], v139 offset:37888
	ds_read_b128 v[198:201], v139 offset:38912
	ds_read_b128 v[202:205], v139 offset:39936
	s_nop 0
	global_load_lds_dwordx4 v0, s[66:67]
	v_mov_b32_e32 v0, v134
	s_mov_b32 m0, s53
	s_nop 0
	global_load_lds_dwordx4 v0, s[66:67]
	s_waitcnt lgkmcnt(8)
	s_barrier
	s_waitcnt lgkmcnt(0)
	s_waitcnt lgkmcnt(0)
	v_mfma_f32_16x16x32_bf16 v[128:131], v[140:143], v[158:161], v[128:131]
	v_mfma_f32_16x16x32_bf16 v[124:127], v[150:153], v[158:161], v[124:127]
	v_mfma_f32_16x16x32_bf16 v[112:115], v[140:143], v[166:169], v[112:115]
	v_mfma_f32_16x16x32_bf16 v[108:111], v[150:153], v[166:169], v[108:111]
	v_mfma_f32_16x16x32_bf16 v[96:99], v[140:143], v[190:193], v[96:99]
	v_mfma_f32_16x16x32_bf16 v[92:95], v[150:153], v[190:193], v[92:95]
	v_mfma_f32_16x16x32_bf16 v[80:83], v[140:143], v[198:201], v[80:83]
	v_mfma_f32_16x16x32_bf16 v[76:79], v[150:153], v[198:201], v[76:79]
	v_mfma_f32_16x16x32_bf16 v[128:131], v[146:149], v[162:165], v[128:131]
	v_mfma_f32_16x16x32_bf16 v[124:127], v[154:157], v[162:165], v[124:127]
	v_mfma_f32_16x16x32_bf16 v[112:115], v[146:149], v[170:173], v[112:115]
	v_mfma_f32_16x16x32_bf16 v[108:111], v[154:157], v[170:173], v[108:111]
	v_mfma_f32_16x16x32_bf16 v[96:99], v[146:149], v[194:197], v[96:99]
	v_mfma_f32_16x16x32_bf16 v[92:95], v[154:157], v[194:197], v[92:95]
	v_mfma_f32_16x16x32_bf16 v[80:83], v[146:149], v[202:205], v[80:83]
	v_mfma_f32_16x16x32_bf16 v[76:79], v[154:157], v[202:205], v[76:79]
	s_barrier
	s_add_i32 s14, 0, 0x1c000
	s_add_u32 s24, s24, 0x80
	v_add_u32_e32 v0, s14, v137
	s_addc_u32 s25, s25, 0
	ds_read_b128 v[206:209], v0
	ds_read_b128 v[210:213], v0 offset:1024
	ds_read_b128 v[214:217], v0 offset:2048
	ds_read_b128 v[218:221], v0 offset:3072
	s_mov_b64 s[66:67], s[24:25]
	v_mov_b32_e32 v0, v133
	s_add_i32 s15, s64, s17
	s_mov_b32 m0, s15
	s_nop 0
	global_load_lds_dwordx4 v0, s[66:67]
	v_mov_b32_e32 v0, v135
	s_add_i32 m0, s15, 0x2000
	s_nop 0
	global_load_lds_dwordx4 v0, s[66:67]
	s_barrier
; template <class Epi, class Sched>
; __device__ __forceinline__ void gemm_phase(LAS unsigned char* lds, const int K_, const Sched& S, const Epi& E, const int wave_) {
;     ...
;         int t = 0;
;         if (Epi::NSTORE > 0 && hoisted) { PG8_BODY(true); t = 2; }
;         for (; t < nt; t += 2) { PG8_BODY(false); }
	s_waitcnt lgkmcnt(0)
	s_waitcnt lgkmcnt(0)
	v_mfma_f32_16x16x32_bf16 v[120:123], v[206:209], v[158:161], v[120:123]
	v_mfma_f32_16x16x32_bf16 v[116:119], v[214:217], v[158:161], v[116:119]
	v_mfma_f32_16x16x32_bf16 v[104:107], v[206:209], v[166:169], v[104:107]
	v_mfma_f32_16x16x32_bf16 v[100:103], v[214:217], v[166:169], v[100:103]
	v_mfma_f32_16x16x32_bf16 v[88:91], v[206:209], v[190:193], v[88:91]
	v_mfma_f32_16x16x32_bf16 v[84:87], v[214:217], v[190:193], v[84:87]
	v_mfma_f32_16x16x32_bf16 v[72:75], v[206:209], v[198:201], v[72:75]
	v_mfma_f32_16x16x32_bf16 v[68:71], v[214:217], v[198:201], v[68:71]
	v_mfma_f32_16x16x32_bf16 v[120:123], v[210:213], v[162:165], v[120:123]
	v_mfma_f32_16x16x32_bf16 v[116:119], v[218:221], v[162:165], v[116:119]
	v_mfma_f32_16x16x32_bf16 v[104:107], v[210:213], v[170:173], v[104:107]
	v_mfma_f32_16x16x32_bf16 v[100:103], v[218:221], v[170:173], v[100:103]
	v_mfma_f32_16x16x32_bf16 v[88:91], v[210:213], v[194:197], v[88:91]
	v_mfma_f32_16x16x32_bf16 v[84:87], v[218:221], v[194:197], v[84:87]
	v_mfma_f32_16x16x32_bf16 v[72:75], v[210:213], v[202:205], v[72:75]
	v_mfma_f32_16x16x32_bf16 v[68:71], v[218:221], v[202:205], v[68:71]
	s_add_u32 s50, s50, 0x80
	s_addc_u32 s51, s51, 0
	v_mov_b32_e32 v0, v132
	s_mov_b32 m0, s55
	s_barrier
	ds_read_b128 v[158:161], v139 offset:49152
	ds_read_b128 v[162:165], v139 offset:50176
	ds_read_b128 v[166:169], v139 offset:51200
	ds_read_b128 v[170:173], v139 offset:52224
	ds_read_b128 v[190:193], v139 offset:53248
	ds_read_b128 v[194:197], v139 offset:54272
	ds_read_b128 v[198:201], v139 offset:55296
	ds_read_b128 v[202:205], v139 offset:56320
	s_nop 0
	global_load_lds_dwordx4 v0, s[50:51]
	v_mov_b32_e32 v0, v134
	s_mov_b32 m0, s56
	s_nop 0
	global_load_lds_dwordx4 v0, s[50:51]
	s_barrier
	s_waitcnt lgkmcnt(0)
	s_waitcnt lgkmcnt(0)
	v_mfma_f32_16x16x32_bf16 v[64:67], v[140:143], v[158:161], v[64:67]
	v_mfma_f32_16x16x32_bf16 v[60:63], v[150:153], v[158:161], v[60:63]
	v_mfma_f32_16x16x32_bf16 v[48:51], v[140:143], v[166:169], v[48:51]
	v_mfma_f32_16x16x32_bf16 v[44:47], v[150:153], v[166:169], v[44:47]
	v_mfma_f32_16x16x32_bf16 v[32:35], v[140:143], v[190:193], v[32:35]
	v_mfma_f32_16x16x32_bf16 v[28:31], v[150:153], v[190:193], v[28:31]
	v_mfma_f32_16x16x32_bf16 v[16:19], v[140:143], v[198:201], v[16:19]
	v_mfma_f32_16x16x32_bf16 v[12:15], v[150:153], v[198:201], v[12:15]
	v_mfma_f32_16x16x32_bf16 v[64:67], v[146:149], v[162:165], v[64:67]
	v_mfma_f32_16x16x32_bf16 v[60:63], v[154:157], v[162:165], v[60:63]
	v_mfma_f32_16x16x32_bf16 v[48:51], v[146:149], v[170:173], v[48:51]
	v_mfma_f32_16x16x32_bf16 v[44:47], v[154:157], v[170:173], v[44:47]
	v_mfma_f32_16x16x32_bf16 v[32:35], v[146:149], v[194:197], v[32:35]
	v_mfma_f32_16x16x32_bf16 v[28:31], v[154:157], v[194:197], v[28:31]
	v_mfma_f32_16x16x32_bf16 v[16:19], v[146:149], v[202:205], v[16:19]
	v_mfma_f32_16x16x32_bf16 v[12:15], v[154:157], v[202:205], v[12:15]
	s_barrier
	s_add_u32 s24, s24, s4
	s_addc_u32 s25, s25, s5
	v_mov_b32_e32 v0, v133
	s_add_i32 s14, s14, s17
	s_mov_b32 m0, s14
	s_nop 0
	global_load_lds_dwordx4 v0, s[24:25]
	v_mov_b32_e32 v0, v135
	s_add_i32 m0, s14, 0x2000
	s_nop 0
	global_load_lds_dwordx4 v0, s[24:25]
	s_waitcnt vmcnt(6)
	s_barrier
	v_mfma_f32_16x16x32_bf16 v[56:59], v[206:209], v[158:161], v[56:59]
	v_mfma_f32_16x16x32_bf16 v[52:55], v[214:217], v[158:161], v[52:55]
	v_mfma_f32_16x16x32_bf16 v[40:43], v[206:209], v[166:169], v[40:43]
	v_mfma_f32_16x16x32_bf16 v[36:39], v[214:217], v[166:169], v[36:39]
	v_mfma_f32_16x16x32_bf16 v[24:27], v[206:209], v[190:193], v[24:27]
	v_mfma_f32_16x16x32_bf16 v[20:23], v[214:217], v[190:193], v[20:23]
	v_mfma_f32_16x16x32_bf16 v[8:11], v[206:209], v[198:201], v[8:11]
	v_mfma_f32_16x16x32_bf16 v[4:7], v[214:217], v[198:201], v[4:7]
	v_mfma_f32_16x16x32_bf16 v[56:59], v[210:213], v[162:165], v[56:59]
	v_mfma_f32_16x16x32_bf16 v[52:55], v[218:221], v[162:165], v[52:55]
	v_mfma_f32_16x16x32_bf16 v[40:43], v[210:213], v[170:173], v[40:43]
	v_mfma_f32_16x16x32_bf16 v[36:39], v[218:221], v[170:173], v[36:39]
	v_mfma_f32_16x16x32_bf16 v[24:27], v[210:213], v[194:197], v[24:27]
	v_mfma_f32_16x16x32_bf16 v[20:23], v[218:221], v[194:197], v[20:23]
	v_mfma_f32_16x16x32_bf16 v[8:11], v[210:213], v[202:205], v[8:11]
	v_mfma_f32_16x16x32_bf16 v[4:7], v[218:221], v[202:205], v[4:7]
	s_add_u32 s29, s29, 0x100
	s_addc_u32 s30, s30, 0
	s_cmp_lt_i32 s31, s54
	s_mov_b32 s24, s31
	s_barrier
	s_cbranch_scc1 .LBB0_1628
	s_mov_b32 s39, 0x8000
	s_and_b64 vcc, exec, s[40:41]
	s_cbranch_vccz .LBB0_1633
	s_branch .LBB0_1634

; template <class Epi, class Sched>
; __device__ __forceinline__ void gemm_phase(LAS unsigned char* lds, const int K_, const Sched& S, const Epi& E, const int wave_) {
;     ...
;         if (Epi::NSTORE > 0 && hoisted) { PG8_BODY(true); t = 2; }
.LBB0_1631:
	s_add_u32 s9, s46, 0x100
	s_addc_u32 s14, s47, 0
	s_and_b64 s[24:25], s[6:7], exec
	s_cselect_b32 s25, s43, s14
	s_cselect_b32 s24, s42, s9
	s_add_i32 s9, 0, 0x10000
	v_add_u32_e32 v0, s9, v137
	ds_read_b128 v[140:143], v0
	ds_read_b128 v[146:149], v0 offset:1024
	ds_read_b128 v[150:153], v0 offset:2048
	ds_read_b128 v[154:157], v0 offset:3072
	ds_read_b128 v[158:161], v139
	ds_read_b128 v[162:165], v139 offset:1024
	ds_read_b128 v[166:169], v139 offset:2048
	ds_read_b128 v[170:173], v139 offset:3072
	ds_read_b128 v[190:193], v139 offset:4096
	ds_read_b128 v[194:197], v139 offset:5120
	ds_read_b128 v[198:201], v139 offset:6144
	ds_read_b128 v[202:205], v139 offset:7168
	s_waitcnt lgkmcnt(8)
	s_barrier
	s_waitcnt lgkmcnt(0)
	s_waitcnt lgkmcnt(0)
	v_mfma_f32_16x16x32_bf16 v[128:131], v[140:143], v[158:161], v[128:131]
	v_mfma_f32_16x16x32_bf16 v[124:127], v[150:153], v[158:161], v[124:127]
	v_mfma_f32_16x16x32_bf16 v[112:115], v[140:143], v[166:169], v[112:115]
	v_mfma_f32_16x16x32_bf16 v[108:111], v[150:153], v[166:169], v[108:111]
	v_mfma_f32_16x16x32_bf16 v[96:99], v[140:143], v[190:193], v[96:99]
	v_mfma_f32_16x16x32_bf16 v[92:95], v[150:153], v[190:193], v[92:95]
	v_mfma_f32_16x16x32_bf16 v[80:83], v[140:143], v[198:201], v[80:83]
	v_mfma_f32_16x16x32_bf16 v[76:79], v[150:153], v[198:201], v[76:79]
	v_mfma_f32_16x16x32_bf16 v[128:131], v[146:149], v[162:165], v[128:131]
	v_mfma_f32_16x16x32_bf16 v[124:127], v[154:157], v[162:165], v[124:127]
	v_mfma_f32_16x16x32_bf16 v[112:115], v[146:149], v[170:173], v[112:115]
	v_mfma_f32_16x16x32_bf16 v[108:111], v[154:157], v[170:173], v[108:111]
	v_mfma_f32_16x16x32_bf16 v[96:99], v[146:149], v[194:197], v[96:99]
	v_mfma_f32_16x16x32_bf16 v[92:95], v[154:157], v[194:197], v[92:95]
	v_mfma_f32_16x16x32_bf16 v[80:83], v[146:149], v[202:205], v[80:83]
	v_mfma_f32_16x16x32_bf16 v[76:79], v[154:157], v[202:205], v[76:79]
	s_barrier
	s_add_i32 s14, 0, 0x14000
	v_add_u32_e32 v0, s14, v137
	ds_read_b128 v[206:209], v0
	ds_read_b128 v[210:213], v0 offset:1024
	ds_read_b128 v[214:217], v0 offset:2048
	ds_read_b128 v[218:221], v0 offset:3072
	s_mov_b64 s[30:31], s[24:25]
	v_mov_b32_e32 v0, v133
	s_add_i32 s9, s9, s17
	s_mov_b32 m0, s9
	s_nop 0
	global_load_lds_dwordx4 v0, s[30:31]
	v_mov_b32_e32 v0, v135
	s_add_i32 m0, s9, 0x2000
	s_nop 0
	global_load_lds_dwordx4 v0, s[30:31]
	s_barrier
	s_waitcnt lgkmcnt(0)
	s_waitcnt lgkmcnt(0)
	v_mfma_f32_16x16x32_bf16 v[120:123], v[206:209], v[158:161], v[120:123]
	v_mfma_f32_16x16x32_bf16 v[116:119], v[214:217], v[158:161], v[116:119]
	v_mfma_f32_16x16x32_bf16 v[104:107], v[206:209], v[166:169], v[104:107]
	v_mfma_f32_16x16x32_bf16 v[100:103], v[214:217], v[166:169], v[100:103]
	v_mfma_f32_16x16x32_bf16 v[88:91], v[206:209], v[190:193], v[88:91]
	v_mfma_f32_16x16x32_bf16 v[84:87], v[214:217], v[190:193], v[84:87]
	v_mfma_f32_16x16x32_bf16 v[72:75], v[206:209], v[198:201], v[72:75]
	v_mfma_f32_16x16x32_bf16 v[68:71], v[214:217], v[198:201], v[68:71]
	v_mfma_f32_16x16x32_bf16 v[120:123], v[210:213], v[162:165], v[120:123]
	v_mfma_f32_16x16x32_bf16 v[116:119], v[218:221], v[162:165], v[116:119]
	v_mfma_f32_16x16x32_bf16 v[104:107], v[210:213], v[170:173], v[104:107]
	v_mfma_f32_16x16x32_bf16 v[100:103], v[218:221], v[170:173], v[100:103]
	v_mfma_f32_16x16x32_bf16 v[88:91], v[210:213], v[194:197], v[88:91]
	v_mfma_f32_16x16x32_bf16 v[84:87], v[218:221], v[194:197], v[84:87]
	v_mfma_f32_16x16x32_bf16 v[72:75], v[210:213], v[202:205], v[72:75]
	v_mfma_f32_16x16x32_bf16 v[68:71], v[218:221], v[202:205], v[68:71]
	s_and_b64 s[30:31], s[6:7], exec
	s_cselect_b32 s15, s44, s48
	s_cselect_b32 s9, s45, s49
	s_add_u32 s50, s15, s58
	s_addc_u32 s51, s9, 0
	s_mov_b64 s[30:31], s[50:51]
	v_mov_b32_e32 v0, v132
	s_mov_b32 m0, s26
	s_barrier
	ds_read_b128 v[158:161], v139 offset:16384
	ds_read_b128 v[162:165], v139 offset:17408
	ds_read_b128 v[166:169], v139 offset:18432
	ds_read_b128 v[170:173], v139 offset:19456
	ds_read_b128 v[190:193], v139 offset:20480
	ds_read_b128 v[194:197], v139 offset:21504
	ds_read_b128 v[198:201], v139 offset:22528
	ds_read_b128 v[202:205], v139 offset:23552
	s_nop 0
	global_load_lds_dwordx4 v0, s[30:31]
	v_mov_b32_e32 v0, v134
	s_mov_b32 m0, s27
	s_nop 0
	global_load_lds_dwordx4 v0, s[30:31]
	s_barrier
	s_waitcnt lgkmcnt(0)
	s_waitcnt lgkmcnt(0)
	v_mfma_f32_16x16x32_bf16 v[64:67], v[140:143], v[158:161], v[64:67]
	v_mfma_f32_16x16x32_bf16 v[60:63], v[150:153], v[158:161], v[60:63]
	v_mfma_f32_16x16x32_bf16 v[48:51], v[140:143], v[166:169], v[48:51]
	v_mfma_f32_16x16x32_bf16 v[44:47], v[150:153], v[166:169], v[44:47]
	v_mfma_f32_16x16x32_bf16 v[32:35], v[140:143], v[190:193], v[32:35]
	v_mfma_f32_16x16x32_bf16 v[28:31], v[150:153], v[190:193], v[28:31]
	v_mfma_f32_16x16x32_bf16 v[16:19], v[140:143], v[198:201], v[16:19]
	v_mfma_f32_16x16x32_bf16 v[12:15], v[150:153], v[198:201], v[12:15]
	v_mfma_f32_16x16x32_bf16 v[64:67], v[146:149], v[162:165], v[64:67]
	v_mfma_f32_16x16x32_bf16 v[60:63], v[154:157], v[162:165], v[60:63]
	v_mfma_f32_16x16x32_bf16 v[48:51], v[146:149], v[170:173], v[48:51]
	v_mfma_f32_16x16x32_bf16 v[44:47], v[154:157], v[170:173], v[44:47]
	v_mfma_f32_16x16x32_bf16 v[32:35], v[146:149], v[194:197], v[32:35]
	v_mfma_f32_16x16x32_bf16 v[28:31], v[154:157], v[194:197], v[28:31]
	v_mfma_f32_16x16x32_bf16 v[16:19], v[146:149], v[202:205], v[16:19]
	v_mfma_f32_16x16x32_bf16 v[12:15], v[154:157], v[202:205], v[12:15]
	s_barrier
	s_add_u32 s30, s24, s4
	s_addc_u32 s31, s25, s5
	v_mov_b32_e32 v0, v133
	s_add_i32 s14, s14, s17
	s_mov_b32 m0, s14
	s_nop 0
	global_load_lds_dwordx4 v0, s[30:31]
	v_mov_b32_e32 v0, v135
	s_add_i32 m0, s14, 0x2000
	s_nop 0
	global_load_lds_dwordx4 v0, s[30:31]
	s_waitcnt vmcnt(14)
	s_barrier
	v_mfma_f32_16x16x32_bf16 v[56:59], v[206:209], v[158:161], v[56:59]
	v_mfma_f32_16x16x32_bf16 v[52:55], v[214:217], v[158:161], v[52:55]
	v_mfma_f32_16x16x32_bf16 v[40:43], v[206:209], v[166:169], v[40:43]
	v_mfma_f32_16x16x32_bf16 v[36:39], v[214:217], v[166:169], v[36:39]
	v_mfma_f32_16x16x32_bf16 v[24:27], v[206:209], v[190:193], v[24:27]
	v_mfma_f32_16x16x32_bf16 v[20:23], v[214:217], v[190:193], v[20:23]
	v_mfma_f32_16x16x32_bf16 v[8:11], v[206:209], v[198:201], v[8:11]
	v_mfma_f32_16x16x32_bf16 v[4:7], v[214:217], v[198:201], v[4:7]
	v_mfma_f32_16x16x32_bf16 v[56:59], v[210:213], v[162:165], v[56:59]
	v_mfma_f32_16x16x32_bf16 v[52:55], v[218:221], v[162:165], v[52:55]
	v_mfma_f32_16x16x32_bf16 v[40:43], v[210:213], v[170:173], v[40:43]
	v_mfma_f32_16x16x32_bf16 v[36:39], v[218:221], v[170:173], v[36:39]
	v_mfma_f32_16x16x32_bf16 v[24:27], v[210:213], v[194:197], v[24:27]
	v_mfma_f32_16x16x32_bf16 v[20:23], v[218:221], v[194:197], v[20:23]
	v_mfma_f32_16x16x32_bf16 v[8:11], v[210:213], v[202:205], v[8:11]
	v_mfma_f32_16x16x32_bf16 v[4:7], v[218:221], v[202:205], v[4:7]
	s_add_i32 s14, 0, 0x18000
	v_add_u32_e32 v0, s14, v137
	s_barrier
	ds_read_b128 v[140:143], v0
	ds_read_b128 v[146:149], v0 offset:1024
	ds_read_b128 v[150:153], v0 offset:2048
	ds_read_b128 v[154:157], v0 offset:3072
	s_add_u32 s15, s15, s0
	s_addc_u32 s9, s9, s1
	s_add_u32 s30, s15, s58
	s_addc_u32 s31, s9, 0
	v_mov_b32_e32 v0, v132
	s_mov_b32 m0, s52
	ds_read_b128 v[158:161], v139 offset:32768
	ds_read_b128 v[162:165], v139 offset:33792
	ds_read_b128 v[166:169], v139 offset:34816
	ds_read_b128 v[170:173], v139 offset:35840
	ds_read_b128 v[190:193], v139 offset:36864
	ds_read_b128 v[194:197], v139 offset:37888
	ds_read_b128 v[198:201], v139 offset:38912
	ds_read_b128 v[202:205], v139 offset:39936
	s_nop 0
	global_load_lds_dwordx4 v0, s[30:31]
	v_mov_b32_e32 v0, v134
	s_mov_b32 m0, s53
	s_nop 0
	global_load_lds_dwordx4 v0, s[30:31]
	s_waitcnt lgkmcnt(8)
	s_barrier
	s_waitcnt lgkmcnt(0)
	s_waitcnt lgkmcnt(0)
	v_mfma_f32_16x16x32_bf16 v[128:131], v[140:143], v[158:161], v[128:131]
	v_mfma_f32_16x16x32_bf16 v[124:127], v[150:153], v[158:161], v[124:127]
	v_mfma_f32_16x16x32_bf16 v[112:115], v[140:143], v[166:169], v[112:115]
	v_mfma_f32_16x16x32_bf16 v[108:111], v[150:153], v[166:169], v[108:111]
	v_mfma_f32_16x16x32_bf16 v[96:99], v[140:143], v[190:193], v[96:99]
	v_mfma_f32_16x16x32_bf16 v[92:95], v[150:153], v[190:193], v[92:95]
	v_mfma_f32_16x16x32_bf16 v[80:83], v[140:143], v[198:201], v[80:83]
	v_mfma_f32_16x16x32_bf16 v[76:79], v[150:153], v[198:201], v[76:79]
	v_mfma_f32_16x16x32_bf16 v[128:131], v[146:149], v[162:165], v[128:131]
	v_mfma_f32_16x16x32_bf16 v[124:127], v[154:157], v[162:165], v[124:127]
	v_mfma_f32_16x16x32_bf16 v[112:115], v[146:149], v[170:173], v[112:115]
	v_mfma_f32_16x16x32_bf16 v[108:111], v[154:157], v[170:173], v[108:111]
	v_mfma_f32_16x16x32_bf16 v[96:99], v[146:149], v[194:197], v[96:99]
	v_mfma_f32_16x16x32_bf16 v[92:95], v[154:157], v[194:197], v[92:95]
	v_mfma_f32_16x16x32_bf16 v[80:83], v[146:149], v[202:205], v[80:83]
	v_mfma_f32_16x16x32_bf16 v[76:79], v[154:157], v[202:205], v[76:79]
	s_barrier
	s_add_i32 s9, 0, 0x1c000
	s_add_u32 s24, s24, 0x80
	v_add_u32_e32 v0, s9, v137
	s_addc_u32 s25, s25, 0
	ds_read_b128 v[206:209], v0
	ds_read_b128 v[210:213], v0 offset:1024
	ds_read_b128 v[214:217], v0 offset:2048
	ds_read_b128 v[218:221], v0 offset:3072
	s_mov_b64 s[30:31], s[24:25]
	v_mov_b32_e32 v0, v133
	s_add_i32 s14, s14, s17
	s_mov_b32 m0, s14
	s_nop 0
	global_load_lds_dwordx4 v0, s[30:31]
	v_mov_b32_e32 v0, v135
	s_add_i32 m0, s14, 0x2000
	s_nop 0
	global_load_lds_dwordx4 v0, s[30:31]
	s_barrier
; template <class Epi, class Sched>
; __device__ __forceinline__ void gemm_phase(LAS unsigned char* lds, const int K_, const Sched& S, const Epi& E, const int wave_) {
;     ...
;         int t = 0;
;         if (Epi::NSTORE > 0 && hoisted) { PG8_BODY(true); t = 2; }
;         for (; t < nt; t += 2) { PG8_BODY(false); }
	s_waitcnt lgkmcnt(0)
	s_waitcnt lgkmcnt(0)
	v_mfma_f32_16x16x32_bf16 v[120:123], v[206:209], v[158:161], v[120:123]
	v_mfma_f32_16x16x32_bf16 v[116:119], v[214:217], v[158:161], v[116:119]
	v_mfma_f32_16x16x32_bf16 v[104:107], v[206:209], v[166:169], v[104:107]
	v_mfma_f32_16x16x32_bf16 v[100:103], v[214:217], v[166:169], v[100:103]
	v_mfma_f32_16x16x32_bf16 v[88:91], v[206:209], v[190:193], v[88:91]
	v_mfma_f32_16x16x32_bf16 v[84:87], v[214:217], v[190:193], v[84:87]
	v_mfma_f32_16x16x32_bf16 v[72:75], v[206:209], v[198:201], v[72:75]
	v_mfma_f32_16x16x32_bf16 v[68:71], v[214:217], v[198:201], v[68:71]
	v_mfma_f32_16x16x32_bf16 v[120:123], v[210:213], v[162:165], v[120:123]
	v_mfma_f32_16x16x32_bf16 v[116:119], v[218:221], v[162:165], v[116:119]
	v_mfma_f32_16x16x32_bf16 v[104:107], v[210:213], v[170:173], v[104:107]
	v_mfma_f32_16x16x32_bf16 v[100:103], v[218:221], v[170:173], v[100:103]
	v_mfma_f32_16x16x32_bf16 v[88:91], v[210:213], v[194:197], v[88:91]
	v_mfma_f32_16x16x32_bf16 v[84:87], v[218:221], v[194:197], v[84:87]
	v_mfma_f32_16x16x32_bf16 v[72:75], v[210:213], v[202:205], v[72:75]
	v_mfma_f32_16x16x32_bf16 v[68:71], v[218:221], v[202:205], v[68:71]
	s_add_u32 s30, s50, 0x80
	s_addc_u32 s31, s51, 0
	v_mov_b32_e32 v0, v132
	s_mov_b32 m0, s55
	s_barrier
	ds_read_b128 v[158:161], v139 offset:49152
	ds_read_b128 v[162:165], v139 offset:50176
	ds_read_b128 v[166:169], v139 offset:51200
	ds_read_b128 v[170:173], v139 offset:52224
	ds_read_b128 v[190:193], v139 offset:53248
	ds_read_b128 v[194:197], v139 offset:54272
	ds_read_b128 v[198:201], v139 offset:55296
	ds_read_b128 v[202:205], v139 offset:56320
	s_nop 0
	global_load_lds_dwordx4 v0, s[30:31]
	v_mov_b32_e32 v0, v134
	s_mov_b32 m0, s56
	s_nop 0
	global_load_lds_dwordx4 v0, s[30:31]
	s_barrier
	s_waitcnt lgkmcnt(0)
	s_waitcnt lgkmcnt(0)
	v_mfma_f32_16x16x32_bf16 v[64:67], v[140:143], v[158:161], v[64:67]
	v_mfma_f32_16x16x32_bf16 v[60:63], v[150:153], v[158:161], v[60:63]
	v_mfma_f32_16x16x32_bf16 v[48:51], v[140:143], v[166:169], v[48:51]
	v_mfma_f32_16x16x32_bf16 v[44:47], v[150:153], v[166:169], v[44:47]
	v_mfma_f32_16x16x32_bf16 v[32:35], v[140:143], v[190:193], v[32:35]
	v_mfma_f32_16x16x32_bf16 v[28:31], v[150:153], v[190:193], v[28:31]
	v_mfma_f32_16x16x32_bf16 v[16:19], v[140:143], v[198:201], v[16:19]
	v_mfma_f32_16x16x32_bf16 v[12:15], v[150:153], v[198:201], v[12:15]
	v_mfma_f32_16x16x32_bf16 v[64:67], v[146:149], v[162:165], v[64:67]
	v_mfma_f32_16x16x32_bf16 v[60:63], v[154:157], v[162:165], v[60:63]
	v_mfma_f32_16x16x32_bf16 v[48:51], v[146:149], v[170:173], v[48:51]
	v_mfma_f32_16x16x32_bf16 v[44:47], v[154:157], v[170:173], v[44:47]
	v_mfma_f32_16x16x32_bf16 v[32:35], v[146:149], v[194:197], v[32:35]
	v_mfma_f32_16x16x32_bf16 v[28:31], v[154:157], v[194:197], v[28:31]
	v_mfma_f32_16x16x32_bf16 v[16:19], v[146:149], v[202:205], v[16:19]
	v_mfma_f32_16x16x32_bf16 v[12:15], v[154:157], v[202:205], v[12:15]
	s_barrier
	s_add_u32 s24, s24, s4
	s_addc_u32 s25, s25, s5
	v_mov_b32_e32 v0, v133
	s_add_i32 s9, s9, s17
	s_mov_b32 m0, s9
	s_nop 0
	global_load_lds_dwordx4 v0, s[24:25]
	v_mov_b32_e32 v0, v135
	s_add_i32 m0, s9, 0x2000
	s_nop 0
	global_load_lds_dwordx4 v0, s[24:25]
	s_waitcnt vmcnt(6)
	s_barrier
	v_mfma_f32_16x16x32_bf16 v[56:59], v[206:209], v[158:161], v[56:59]
	v_mfma_f32_16x16x32_bf16 v[52:55], v[214:217], v[158:161], v[52:55]
	v_mfma_f32_16x16x32_bf16 v[40:43], v[206:209], v[166:169], v[40:43]
	v_mfma_f32_16x16x32_bf16 v[36:39], v[214:217], v[166:169], v[36:39]
	v_mfma_f32_16x16x32_bf16 v[24:27], v[206:209], v[190:193], v[24:27]
	v_mfma_f32_16x16x32_bf16 v[20:23], v[214:217], v[190:193], v[20:23]
	v_mfma_f32_16x16x32_bf16 v[8:11], v[206:209], v[198:201], v[8:11]
	v_mfma_f32_16x16x32_bf16 v[4:7], v[214:217], v[198:201], v[4:7]
	v_mfma_f32_16x16x32_bf16 v[56:59], v[210:213], v[162:165], v[56:59]
	v_mfma_f32_16x16x32_bf16 v[52:55], v[218:221], v[162:165], v[52:55]
	v_mfma_f32_16x16x32_bf16 v[40:43], v[210:213], v[170:173], v[40:43]
	v_mfma_f32_16x16x32_bf16 v[36:39], v[218:221], v[170:173], v[36:39]
	v_mfma_f32_16x16x32_bf16 v[24:27], v[210:213], v[194:197], v[24:27]
	v_mfma_f32_16x16x32_bf16 v[20:23], v[218:221], v[194:197], v[20:23]
	v_mfma_f32_16x16x32_bf16 v[8:11], v[210:213], v[202:205], v[8:11]
	v_mfma_f32_16x16x32_bf16 v[4:7], v[218:221], v[202:205], v[4:7]
	s_mov_b32 s24, 2
	s_barrier
	s_cmp_ge_i32 s24, s54
	s_cbranch_scc0 .LBB0_1627
